# baseline (speedup 1.0000x reference)
_Z16closed_form_mainPKfS0_PKiPf:
	s_load_dwordx8 s[16:23], s[0:1], 0x0
	s_lshr_b32 s6, s2, 3
	v_readfirstlane_b32 s0, v0
	s_mul_hi_u32 s7, s6, 0x24924925
	s_lshr_b32 s4, s0, 6
	s_and_b32 s0, s2, 7
	s_mul_i32 s1, s7, 7
	s_bfe_u32 s5, s2, 0x10003
	s_sub_i32 s1, s6, s1
	s_mul_i32 s36, s0, 7
	s_xor_b32 s3, s4, s5
	s_add_i32 s36, s36, s1
	s_waitcnt lgkmcnt(0)
	s_mov_b64 s[28:29], s[22:23]
	v_and_b32_e32 v19, 63, v0
	s_cmp_lt_u32 s36, 52
	s_mov_b64 s[0:1], -1
	s_cbranch_scc0 .LBB0_32
	s_mul_hi_u32 s0, s6, 0x20820821
	s_lshr_b32 s38, s0, 3
	s_mul_hi_u32 s0, s7, 0x1c71c71d
	s_mul_i32 s0, s0, 9
	s_sub_i32 s0, s7, s0
	v_add_u32_e32 v2, -3, v19
	v_mad_u64_u32 v[0:1], s[0:1], s0, 57, v[2:3]
	s_mov_b64 s[24:25], s[18:19]
	v_mov_b32_e32 v1, 0x200
	v_med3_i32 v1, v0, 0, v1
	s_mul_i32 s34, s36, 10
	s_and_b32 s17, s17, 0xffff
	s_and_b32 s25, s25, 0xffff
	v_cmp_gt_u32_e64 s[0:1], 57, v2
	s_mov_b32 s19, 0x20000
	s_mov_b32 s18, 0xe0e038
	s_mov_b32 s26, 0x606018
	s_mul_i32 s35, s38, 0x70701c
	s_mul_i32 s33, s38, 0x30300c
	v_lshlrev_b32_e32 v28, 2, v1
	v_mul_u32_u24_e32 v27, 12, v1
	v_lshlrev_b32_e32 v23, 4, v19
	s_cmp_lg_u32 s4, s5
	v_sub_u32_e64 v29, s34, 2 clamp
	s_cbranch_scc0 .LBB0_15
	s_setprio 2
	s_mov_b32 s27, s19
	s_and_b32 s21, s21, 0xffff
	s_mov_b32 s22, 0x202008
	s_mov_b32 s23, s19
	s_mul_i32 s38, s38, 0x101004
	s_movk_i32 s37, 0x80
	v_add_u32_e32 v18, -1, v0
	s_movk_i32 s4, 0x201
	s_movk_i32 s5, 0x1ff
	v_cmp_gt_u32_e64 s[40:41], s4, v0
	v_cmp_gt_u32_e64 s[42:43], s5, v18
	v_mov_b32_e32 v18, 0x42c80000
	v_mov_b32_e32 v22, 0x3de38e39
	v_mov_b32_e32 v26, 0x3a3d6628
	v_mov_b32_e32 v1, 0
	s_add_i32 s4, s34, -3
	s_max_i32 s4, s4, 0
	s_mul_i32 s4, s4, 0x804
	s_add_i32 s4, s4, s38
	buffer_load_dword v29, v28, s[20:23], s4 offen nt
	s_add_i32 s4, s34, -2
	s_max_i32 s4, s4, 0
	s_mul_i32 s4, s4, 0x804
	s_add_i32 s4, s4, s38
	buffer_load_dword v2, v28, s[20:23], s4 offen nt
	s_add_i32 s5, s34, -2
	s_max_i32 s5, s5, 0
	s_mul_i32 s6, s5, 0x804
	s_add_i32 s6, s6, s35
	s_add_i32 s7, s6, 0x505014
	s_add_i32 s8, s6, 0x606018
	s_mul_i32 s9, s5, 0x180c
	s_add_i32 s9, s9, s33
	s_add_i32 s4, s34, -1
	s_max_i32 s4, s4, 0
	s_mul_i32 s4, s4, 0x804
	s_add_i32 s4, s4, s38
	buffer_load_dword v3, v28, s[20:23], s4 offen nt
	buffer_load_dwordx3 v[8:10], v27, s[24:27], s9 offen nt
	buffer_load_dword v4, v28, s[16:19], s7 offen nt
	buffer_load_dword v5, v28, s[16:19], s8 offen nt
	s_add_i32 s5, s34, -1
	s_max_i32 s5, s5, 0
	s_mul_i32 s6, s5, 0x804
	s_add_i32 s6, s6, s35
	s_add_i32 s7, s6, 0x505014
	s_add_i32 s8, s6, 0x606018
	s_mul_i32 s9, s5, 0x180c
	s_add_i32 s9, s9, s33
	s_add_i32 s4, s34, 0
	s_min_i32 s4, s4, 0x200
	s_mul_i32 s4, s4, 0x804
	s_add_i32 s4, s4, s38
	buffer_load_dword v16, v28, s[20:23], s4 offen nt
	buffer_load_dwordx3 v[12:14], v27, s[24:27], s9 offen nt
	buffer_load_dword v6, v28, s[16:19], s7 offen nt
	buffer_load_dword v7, v28, s[16:19], s8 offen nt
	s_add_i32 s5, s34, 0
	s_min_i32 s5, s5, 0x200
	s_mul_i32 s6, s5, 0x804
	s_add_i32 s6, s6, s35
	s_add_i32 s7, s6, 0x505014
	s_add_i32 s8, s6, 0x606018
	s_mul_i32 s9, s5, 0x180c
	s_add_i32 s9, s9, s33
	s_add_i32 s4, s34, 1
	s_min_i32 s4, s4, 0x200
	s_mul_i32 s4, s4, 0x804
	s_add_i32 s4, s4, s38
	buffer_load_dword v17, v28, s[20:23], s4 offen nt
	buffer_load_dwordx3 v[32:34], v27, s[24:27], s9 offen nt
	buffer_load_dword v20, v28, s[16:19], s7 offen nt
	buffer_load_dword v21, v28, s[16:19], s8 offen nt
	s_waitcnt vmcnt(12)
	s_add_i32 s4, s34, -3
	s_cmpk_lt_u32 s4, 0x201
	s_cselect_b64 s[12:13], s[40:41], 0
	v_cmp_eq_u32_e64 s[14:15], s37, v29
	s_and_b64 s[14:15], s[14:15], s[12:13]
	v_cndmask_b32_e64 v24, 0, 1, s[14:15]
	s_add_i32 s4, s34, -2
	s_cmpk_lt_u32 s4, 0x201
	s_cselect_b64 s[12:13], s[40:41], 0
	v_cmp_eq_u32_e64 s[14:15], s37, v2
	s_and_b64 s[14:15], s[14:15], s[12:13]
	v_cndmask_b32_e64 v25, 0, 1, s[14:15]
	s_nop 0
	v_or_b32_dpp v30, v24, v24 wave_shr:1 row_mask:0xf bank_mask:0xf bound_ctrl:1
	v_or_b32_dpp v31, v25, v25 wave_shr:1 row_mask:0xf bank_mask:0xf bound_ctrl:1
	s_nop 1
	v_or_b32_dpp v30, v24, v30 wave_shl:1 row_mask:0xf bank_mask:0xf bound_ctrl:1
	v_or_b32_dpp v31, v25, v31 wave_shl:1 row_mask:0xf bank_mask:0xf bound_ctrl:1
	s_nop 1
	v_or_b32_dpp v36, v30, v30 wave_shr:1 row_mask:0xf bank_mask:0xf bound_ctrl:1
	v_or_b32_dpp v37, v31, v31 wave_shr:1 row_mask:0xf bank_mask:0xf bound_ctrl:1
	s_nop 1
	v_or_b32_dpp v36, v30, v36 wave_shl:1 row_mask:0xf bank_mask:0xf bound_ctrl:1
	v_or_b32_dpp v37, v31, v37 wave_shl:1 row_mask:0xf bank_mask:0xf bound_ctrl:1
	v_mov_b32_e32 v24, 0
	v_mov_b32_e32 v25, 0
	s_waitcnt vmcnt(8)
	v_mov_b32_dpp v40, v8 wave_shr:1 row_mask:0xf bank_mask:0xf bound_ctrl:1
	v_mov_b32_dpp v41, v9 wave_shr:1 row_mask:0xf bank_mask:0xf bound_ctrl:1
	v_mov_b32_dpp v42, v10 wave_shr:1 row_mask:0xf bank_mask:0xf bound_ctrl:1
	v_mov_b32_dpp v44, v8 wave_shl:1 row_mask:0xf bank_mask:0xf bound_ctrl:1
	v_mov_b32_dpp v45, v9 wave_shl:1 row_mask:0xf bank_mask:0xf bound_ctrl:1
	v_mov_b32_dpp v46, v10 wave_shl:1 row_mask:0xf bank_mask:0xf bound_ctrl:1
	s_add_i32 s4, s34, -1
	s_cmpk_lt_u32 s4, 0x201
	s_cselect_b64 s[12:13], s[40:41], 0
	v_cmp_eq_u32_e64 s[14:15], s37, v3
	s_and_b64 s[14:15], s[14:15], s[12:13]
	v_cndmask_b32_e64 v30, 0, 1, s[14:15]
	v_pk_add_f32 v[38:39], v[8:9], v[40:41]
	v_pk_mul_f32 v[48:49], v[8:9], v[8:9] op_sel_hi:[0,1]
	v_or_b32_dpp v31, v30, v30 wave_shr:1 row_mask:0xf bank_mask:0xf bound_ctrl:1
	v_pk_mul_f32 v[50:51], v[8:9], v[10:11] op_sel_hi:[1,0]
	v_or_b32_dpp v31, v30, v31 wave_shl:1 row_mask:0xf bank_mask:0xf bound_ctrl:1
	v_mul_f32_e64 v52, v9, v9
	v_mul_f32_e64 v53, v10, v10
	v_or_b32_dpp v56, v31, v31 wave_shr:1 row_mask:0xf bank_mask:0xf bound_ctrl:1
	v_add_f32_e64 v54, v10, v42
	v_pk_add_f32 v[38:39], v[38:39], v[44:45]
	v_or_b32_dpp v56, v31, v56 wave_shl:1 row_mask:0xf bank_mask:0xf bound_ctrl:1
	v_or3_b32 v57, v56, v37, v36
	v_or3_b32 v57, v57, v24, v25
	s_add_i32 s4, s34, -4
	s_cmpk_lt_u32 s4, 0x1ff
	s_cselect_b64 s[12:13], s[42:43], 0
	v_cmp_ne_u32_e64 s[30:31], 0, v57
	s_and_b64 s[30:31], s[30:31], s[12:13]
	v_cndmask_b32_e64 v57, 0, 1.0, s[30:31]
	v_pk_fma_f32 v[48:49], v[40:41], v[40:41], v[48:49] op_sel_hi:[0,1,1]
	v_pk_fma_f32 v[50:51], v[40:41], v[42:43], v[50:51] op_sel_hi:[1,0,1]
	v_fma_f32 v52, v41, v41, v52
	v_fma_f32 v53, v42, v42, v53
	v_add_f32_dpp v55, v57, v57 wave_shr:1 row_mask:0xf bank_mask:0xf bound_ctrl:1
	v_add_f32_e64 v54, v54, v46
	v_pk_fma_f32 v[48:49], v[44:45], v[44:45], v[48:49] op_sel_hi:[0,1,1]
	v_pk_fma_f32 v[50:51], v[44:45], v[46:47], v[50:51] op_sel_hi:[1,0,1]
	v_fma_f32 v52, v45, v45, v52
	v_fma_f32 v53, v46, v46, v53
	v_add_f32_dpp v55, v57, v55 wave_shl:1 row_mask:0xf bank_mask:0xf bound_ctrl:1
	v_mov_b32_dpp v30, v4 wave_shr:1 row_mask:0xf bank_mask:0xf bound_ctrl:1
	v_mov_b32_dpp v31, v5 wave_shr:1 row_mask:0xf bank_mask:0xf bound_ctrl:1
	v_mov_b32_dpp v58, v4 wave_shl:1 row_mask:0xf bank_mask:0xf bound_ctrl:1
	v_mov_b32_dpp v59, v5 wave_shl:1 row_mask:0xf bank_mask:0xf bound_ctrl:1
	v_pk_mul_f32 v[60:61], v[4:5], v[8:9] op_sel_hi:[1,0]
	v_pk_mul_f32 v[64:65], v[4:5], v[8:9] op_sel:[0,1]
	v_pk_mul_f32 v[68:69], v[4:5], v[10:11] op_sel_hi:[1,0]
	v_pk_add_f32 v[72:73], v[4:5], v[30:31]
	v_pk_fma_f32 v[60:61], v[30:31], v[40:41], v[60:61] op_sel_hi:[1,0,1]
	v_pk_fma_f32 v[64:65], v[30:31], v[40:41], v[64:65] op_sel:[0,1,0]
	v_pk_fma_f32 v[68:69], v[30:31], v[42:43], v[68:69] op_sel_hi:[1,0,1]
	v_pk_add_f32 v[72:73], v[72:73], v[58:59]
	v_pk_fma_f32 v[60:61], v[58:59], v[44:45], v[60:61] op_sel_hi:[1,0,1]
	v_pk_fma_f32 v[64:65], v[58:59], v[44:45], v[64:65] op_sel:[0,1,0]
	v_pk_fma_f32 v[68:69], v[58:59], v[46:47], v[68:69] op_sel_hi:[1,0,1]
	s_barrier
	s_add_i32 s5, s34, 1
	s_min_i32 s5, s5, 0x200
	s_mul_i32 s6, s5, 0x804
	s_add_i32 s6, s6, s35
	s_add_i32 s7, s6, 0x505014
	s_add_i32 s8, s6, 0x606018
	s_mul_i32 s9, s5, 0x180c
	s_add_i32 s9, s9, s33
	s_add_i32 s4, s34, 2
	s_min_i32 s4, s4, 0x200
	s_mul_i32 s4, s4, 0x804
	s_add_i32 s4, s4, s38
	buffer_load_dword v25, v28, s[20:23], s4 offen nt
	buffer_load_dwordx3 v[76:78], v27, s[24:27], s9 offen nt
	buffer_load_dword v30, v28, s[16:19], s7 offen nt
	buffer_load_dword v31, v28, s[16:19], s8 offen nt
	s_waitcnt vmcnt(8)
	s_add_i32 s4, s34, 0
	s_cmpk_lt_u32 s4, 0x201
	s_cselect_b64 s[12:13], s[40:41], 0
	v_cmp_eq_u32_e64 s[14:15], s37, v16
	s_and_b64 s[14:15], s[14:15], s[12:13]
	v_cndmask_b32_e64 v57, 0, 1, s[14:15]
	s_nop 1
	v_or_b32_dpp v58, v57, v57 wave_shr:1 row_mask:0xf bank_mask:0xf bound_ctrl:1
	s_nop 1
	v_or_b32_dpp v58, v57, v58 wave_shl:1 row_mask:0xf bank_mask:0xf bound_ctrl:1
	s_nop 1
	v_or_b32_dpp v59, v58, v58 wave_shr:1 row_mask:0xf bank_mask:0xf bound_ctrl:1
	s_nop 1
	v_or_b32_dpp v59, v58, v59 wave_shl:1 row_mask:0xf bank_mask:0xf bound_ctrl:1
	s_waitcnt vmcnt(8)
	v_mov_b32_dpp v80, v12 wave_shr:1 row_mask:0xf bank_mask:0xf bound_ctrl:1
	v_mov_b32_dpp v81, v13 wave_shr:1 row_mask:0xf bank_mask:0xf bound_ctrl:1
	v_mov_b32_dpp v82, v14 wave_shr:1 row_mask:0xf bank_mask:0xf bound_ctrl:1
	v_mov_b32_dpp v84, v12 wave_shl:1 row_mask:0xf bank_mask:0xf bound_ctrl:1
	v_mov_b32_dpp v85, v13 wave_shl:1 row_mask:0xf bank_mask:0xf bound_ctrl:1
	v_mov_b32_dpp v86, v14 wave_shl:1 row_mask:0xf bank_mask:0xf bound_ctrl:1
	v_pk_add_f32 v[62:63], v[12:13], v[80:81]
	v_pk_mul_f32 v[66:67], v[12:13], v[12:13] op_sel_hi:[0,1]
	v_pk_mul_f32 v[70:71], v[12:13], v[14:15] op_sel_hi:[1,0]
	v_mul_f32_e64 v74, v13, v13
	v_mul_f32_e64 v75, v14, v14
	v_add_f32_e64 v88, v14, v82
	v_pk_add_f32 v[62:63], v[62:63], v[84:85]
	v_or3_b32 v57, v59, v56, v37
	v_or3_b32 v57, v57, v36, v24
	s_add_i32 s4, s34, -3
	s_cmpk_lt_u32 s4, 0x1ff
	s_cselect_b64 s[12:13], s[42:43], 0
	v_cmp_ne_u32_e64 s[30:31], 0, v57
	s_and_b64 s[30:31], s[30:31], s[12:13]
	v_cndmask_b32_e64 v57, 0, 1.0, s[30:31]
	v_pk_fma_f32 v[66:67], v[80:81], v[80:81], v[66:67] op_sel_hi:[0,1,1]
	v_pk_fma_f32 v[70:71], v[80:81], v[82:83], v[70:71] op_sel_hi:[1,0,1]
	v_fma_f32 v74, v81, v81, v74
	v_fma_f32 v75, v82, v82, v75
	v_add_f32_dpp v89, v57, v57 wave_shr:1 row_mask:0xf bank_mask:0xf bound_ctrl:1
	v_add_f32_e64 v88, v88, v86
	v_pk_fma_f32 v[66:67], v[84:85], v[84:85], v[66:67] op_sel_hi:[0,1,1]
	v_pk_fma_f32 v[70:71], v[84:85], v[86:87], v[70:71] op_sel_hi:[1,0,1]
	v_fma_f32 v74, v85, v85, v74
	v_fma_f32 v75, v86, v86, v75
	v_add_f32_dpp v89, v57, v89 wave_shl:1 row_mask:0xf bank_mask:0xf bound_ctrl:1
	v_mov_b32_dpp v92, v6 wave_shr:1 row_mask:0xf bank_mask:0xf bound_ctrl:1
	v_mov_b32_dpp v93, v7 wave_shr:1 row_mask:0xf bank_mask:0xf bound_ctrl:1
	v_mov_b32_dpp v96, v6 wave_shl:1 row_mask:0xf bank_mask:0xf bound_ctrl:1
	v_mov_b32_dpp v97, v7 wave_shl:1 row_mask:0xf bank_mask:0xf bound_ctrl:1
	v_pk_mul_f32 v[90:91], v[6:7], v[12:13] op_sel_hi:[1,0]
	v_pk_mul_f32 v[94:95], v[6:7], v[12:13] op_sel:[0,1]
	v_pk_mul_f32 v[98:99], v[6:7], v[14:15] op_sel_hi:[1,0]
	v_pk_add_f32 v[102:103], v[6:7], v[92:93]
	v_pk_fma_f32 v[90:91], v[92:93], v[80:81], v[90:91] op_sel_hi:[1,0,1]
	v_pk_fma_f32 v[94:95], v[92:93], v[80:81], v[94:95] op_sel:[0,1,0]
	v_pk_fma_f32 v[98:99], v[92:93], v[82:83], v[98:99] op_sel_hi:[1,0,1]
	v_pk_add_f32 v[102:103], v[102:103], v[96:97]
	v_pk_fma_f32 v[90:91], v[96:97], v[84:85], v[90:91] op_sel_hi:[1,0,1]
	v_pk_fma_f32 v[94:95], v[96:97], v[84:85], v[94:95] op_sel:[0,1,0]
	v_pk_fma_f32 v[98:99], v[96:97], v[86:87], v[98:99] op_sel_hi:[1,0,1]
	s_barrier
	s_add_i32 s5, s34, 2
	s_min_i32 s5, s5, 0x200
	s_mul_i32 s6, s5, 0x804
	s_add_i32 s6, s6, s35
	s_add_i32 s7, s6, 0x505014
	s_add_i32 s8, s6, 0x606018
	s_mul_i32 s9, s5, 0x180c
	s_add_i32 s9, s9, s33
	s_add_i32 s4, s34, 3
	s_min_i32 s4, s4, 0x200
	s_mul_i32 s4, s4, 0x804
	s_add_i32 s4, s4, s38
	buffer_load_dword v24, v28, s[20:23], s4 offen nt
	buffer_load_dwordx3 v[104:106], v27, s[24:27], s9 offen nt
	buffer_load_dword v92, v28, s[16:19], s7 offen nt
	buffer_load_dword v93, v28, s[16:19], s8 offen nt
	s_waitcnt vmcnt(8)
	s_add_i32 s4, s34, 1
	s_cmpk_lt_u32 s4, 0x201
	s_cselect_b64 s[12:13], s[40:41], 0
	v_cmp_eq_u32_e64 s[14:15], s37, v17
	s_and_b64 s[14:15], s[14:15], s[12:13]
	v_cndmask_b32_e64 v29, 0, 1, s[14:15]
	s_nop 1
	v_or_b32_dpp v57, v29, v29 wave_shr:1 row_mask:0xf bank_mask:0xf bound_ctrl:1
	s_nop 1
	v_or_b32_dpp v57, v29, v57 wave_shl:1 row_mask:0xf bank_mask:0xf bound_ctrl:1
	s_nop 1
	v_or_b32_dpp v58, v57, v57 wave_shr:1 row_mask:0xf bank_mask:0xf bound_ctrl:1
	s_nop 1
	v_or_b32_dpp v58, v57, v58 wave_shl:1 row_mask:0xf bank_mask:0xf bound_ctrl:1
	s_waitcnt vmcnt(8)
	v_mov_b32_dpp v108, v32 wave_shr:1 row_mask:0xf bank_mask:0xf bound_ctrl:1
	v_mov_b32_dpp v109, v33 wave_shr:1 row_mask:0xf bank_mask:0xf bound_ctrl:1
	v_mov_b32_dpp v110, v34 wave_shr:1 row_mask:0xf bank_mask:0xf bound_ctrl:1
	v_mov_b32_dpp v112, v32 wave_shl:1 row_mask:0xf bank_mask:0xf bound_ctrl:1
	v_mov_b32_dpp v113, v33 wave_shl:1 row_mask:0xf bank_mask:0xf bound_ctrl:1
	v_mov_b32_dpp v114, v34 wave_shl:1 row_mask:0xf bank_mask:0xf bound_ctrl:1
	v_pk_add_f32 v[96:97], v[32:33], v[108:109]
	v_pk_mul_f32 v[100:101], v[32:33], v[32:33] op_sel_hi:[0,1]
	v_pk_mul_f32 v[116:117], v[32:33], v[34:35] op_sel_hi:[1,0]
	v_mul_f32_e64 v118, v33, v33
	v_mul_f32_e64 v119, v34, v34
	v_add_f32_e64 v120, v34, v110
	v_pk_add_f32 v[96:97], v[96:97], v[112:113]
	v_or3_b32 v29, v58, v59, v56
	v_or3_b32 v29, v29, v37, v36
	s_add_i32 s4, s34, -2
	s_cmpk_lt_u32 s4, 0x1ff
	s_cselect_b64 s[12:13], s[42:43], 0
	v_cmp_ne_u32_e64 s[30:31], 0, v29
	s_and_b64 s[30:31], s[30:31], s[12:13]
	v_cndmask_b32_e64 v29, 0, 1.0, s[30:31]
	v_pk_fma_f32 v[100:101], v[108:109], v[108:109], v[100:101] op_sel_hi:[0,1,1]
	v_pk_fma_f32 v[116:117], v[108:109], v[110:111], v[116:117] op_sel_hi:[1,0,1]
	v_fma_f32 v118, v109, v109, v118
	v_fma_f32 v119, v110, v110, v119
	v_add_f32_dpp v121, v29, v29 wave_shr:1 row_mask:0xf bank_mask:0xf bound_ctrl:1
	v_add_f32_e64 v120, v120, v114
	v_pk_fma_f32 v[100:101], v[112:113], v[112:113], v[100:101] op_sel_hi:[0,1,1]
	v_pk_fma_f32 v[116:117], v[112:113], v[114:115], v[116:117] op_sel_hi:[1,0,1]
	v_fma_f32 v118, v113, v113, v118
	v_fma_f32 v119, v114, v114, v119
	v_add_f32_dpp v121, v29, v121 wave_shl:1 row_mask:0xf bank_mask:0xf bound_ctrl:1
	v_pk_add_f32 v[124:125], v[62:63], v[96:97]
	v_pk_add_f32 v[122:123], v[38:39], v[124:125]
	v_pk_add_f32 v[38:39], v[66:67], v[100:101]
	v_pk_add_f32 v[62:63], v[48:49], v[38:39]
	v_pk_add_f32 v[48:49], v[70:71], v[116:117]
	v_pk_add_f32 v[66:67], v[50:51], v[48:49]
	v_pk_add_f32 v[50:51], v[74:75], v[118:119]
	v_pk_add_f32 v[70:71], v[52:53], v[50:51]
	v_pk_add_f32 v[52:53], v[88:89], v[120:121]
	v_pk_add_f32 v[74:75], v[54:55], v[52:53]
	v_mul_f32_e64 v128, v122, v22
	v_mul_f32_e64 v129, v123, v22
	v_mul_f32_e64 v130, v74, v22
	v_fma_f32 v29, v62, v22, v26
	v_mul_f32_e64 v57, v63, v22
	v_mul_f32_e64 v54, v66, v22
	v_fma_f32 v55, v70, v22, v26
	v_mul_f32_e64 v88, v67, v22
	v_fma_f32 v89, v71, v22, v26
	v_fma_f32 v29, -v128, v128, v29
	v_fma_f32 v57, -v128, v129, v57
	v_fma_f32 v54, -v128, v130, v54
	v_fma_f32 v55, -v129, v129, v55
	v_fma_f32 v88, -v129, v130, v88
	v_fma_f32 v89, -v130, v130, v89
	v_mul_f32_e64 v126, v88, v88
	v_mul_f32_e64 v127, v57, v89
	v_mul_f32_e64 v140, v54, v55
	v_mul_f32_e64 v141, v54, v54
	v_mul_f32_e64 v142, v29, v88
	v_mul_f32_e64 v143, v57, v57
	v_fma_f32 v126, v55, v89, -v126
	v_fma_f32 v127, v54, v88, -v127
	v_fma_f32 v140, v57, v88, -v140
	v_fma_f32 v141, v29, v89, -v141
	v_fma_f32 v142, v57, v54, -v142
	v_fma_f32 v143, v29, v55, -v143
	v_mul_f32_e64 v144, v29, v126
	v_fma_f32 v144, v57, v127, v144
	v_fma_f32 v144, v54, v140, v144
	v_rcp_f32_e32 v144, v144
	v_cmp_ne_u32_e64 vcc, s37, v2
	v_mul_f32_e64 v144, v144, v22
	v_cndmask_b32_e64 v144, 0, v144, s[30:31]
	v_cndmask_b32_e64 v29, 0, v18, vcc
	v_cndmask_b32_e64 v137, 0, v22, s[30:31]
	v_mul_f32_e64 v131, v126, v144
	v_mul_f32_e64 v132, v127, v144
	v_mul_f32_e64 v133, v140, v144
	v_mul_f32_e64 v134, v141, v144
	v_mul_f32_e64 v135, v142, v144
	v_mul_f32_e64 v136, v143, v144
	v_add_f32_e64 v138, v75, v29
	v_mov_b32_e32 v139, v2
	ds_write_b128 v23, v[128:131]
	ds_write_b128 v23, v[132:135] offset:1024
	ds_write_b128 v23, v[136:139] offset:2048
	v_mov_b32_dpp v54, v20 wave_shr:1 row_mask:0xf bank_mask:0xf bound_ctrl:1
	v_mov_b32_dpp v55, v21 wave_shr:1 row_mask:0xf bank_mask:0xf bound_ctrl:1
	v_mov_b32_dpp v62, v20 wave_shl:1 row_mask:0xf bank_mask:0xf bound_ctrl:1
	v_mov_b32_dpp v63, v21 wave_shl:1 row_mask:0xf bank_mask:0xf bound_ctrl:1
	v_pk_mul_f32 v[88:89], v[20:21], v[32:33] op_sel_hi:[1,0]
	v_pk_mul_f32 v[140:141], v[20:21], v[32:33] op_sel:[0,1]
	v_pk_mul_f32 v[144:145], v[20:21], v[34:35] op_sel_hi:[1,0]
	v_pk_add_f32 v[148:149], v[20:21], v[54:55]
	v_pk_fma_f32 v[88:89], v[54:55], v[108:109], v[88:89] op_sel_hi:[1,0,1]
	v_pk_fma_f32 v[140:141], v[54:55], v[108:109], v[140:141] op_sel:[0,1,0]
	v_pk_fma_f32 v[144:145], v[54:55], v[110:111], v[144:145] op_sel_hi:[1,0,1]
	v_pk_add_f32 v[148:149], v[148:149], v[62:63]
	v_pk_fma_f32 v[88:89], v[62:63], v[112:113], v[88:89] op_sel_hi:[1,0,1]
	v_pk_fma_f32 v[140:141], v[62:63], v[112:113], v[140:141] op_sel:[0,1,0]
	v_pk_fma_f32 v[144:145], v[62:63], v[114:115], v[144:145] op_sel_hi:[1,0,1]
	s_waitcnt lgkmcnt(0)
	s_barrier
	s_add_i32 s5, s34, 3
	s_min_i32 s5, s5, 0x200
	s_mul_i32 s6, s5, 0x804
	s_add_i32 s6, s6, s35
	s_add_i32 s7, s6, 0x505014
	s_add_i32 s8, s6, 0x606018
	s_mul_i32 s9, s5, 0x180c
	s_add_i32 s9, s9, s33
	s_add_i32 s4, s34, 4
	s_min_i32 s4, s4, 0x200
	s_mul_i32 s4, s4, 0x804
	s_add_i32 s4, s4, s38
	buffer_load_dword v2, v28, s[20:23], s4 offen nt
	buffer_load_dwordx3 v[152:154], v27, s[24:27], s9 offen nt
	buffer_load_dword v54, v28, s[16:19], s7 offen nt
	buffer_load_dword v55, v28, s[16:19], s8 offen nt
	s_waitcnt vmcnt(8)
	s_add_i32 s4, s34, 2
	s_cmpk_lt_u32 s4, 0x201
	s_cselect_b64 s[12:13], s[40:41], 0
	v_cmp_eq_u32_e64 s[14:15], s37, v25
	s_and_b64 s[14:15], s[14:15], s[12:13]
	v_cndmask_b32_e64 v29, 0, 1, s[14:15]
	s_nop 1
	v_or_b32_dpp v36, v29, v29 wave_shr:1 row_mask:0xf bank_mask:0xf bound_ctrl:1
	s_nop 1
	v_or_b32_dpp v36, v29, v36 wave_shl:1 row_mask:0xf bank_mask:0xf bound_ctrl:1
	s_nop 1
	v_or_b32_dpp v57, v36, v36 wave_shr:1 row_mask:0xf bank_mask:0xf bound_ctrl:1
	s_nop 1
	v_or_b32_dpp v57, v36, v57 wave_shl:1 row_mask:0xf bank_mask:0xf bound_ctrl:1
	v_pk_add_f32 v[62:63], v[102:103], v[148:149]
	v_pk_add_f32 v[66:67], v[72:73], v[62:63]
	v_pk_add_f32 v[70:71], v[90:91], v[88:89]
	v_pk_add_f32 v[72:73], v[60:61], v[70:71]
	v_pk_add_f32 v[74:75], v[94:95], v[140:141]
	v_pk_add_f32 v[60:61], v[64:65], v[74:75]
	v_pk_add_f32 v[90:91], v[98:99], v[144:145]
	v_pk_add_f32 v[64:65], v[68:69], v[90:91]
	v_pk_fma_f32 v[72:73], v[128:129], v[66:67], v[72:73] op_sel_hi:[0,1,1] neg_lo:[1,0,0] neg_hi:[1,0,0]
	v_pk_fma_f32 v[60:61], v[128:129], v[66:67], v[60:61] op_sel:[1,0,0] neg_lo:[1,0,0] neg_hi:[1,0,0]
	v_pk_fma_f32 v[64:65], v[130:131], v[66:67], v[64:65] op_sel_hi:[0,1,1] neg_lo:[1,0,0] neg_hi:[1,0,0]
	v_pk_mul_f32 v[94:95], v[130:131], v[72:73] op_sel:[1,0]
	v_pk_mul_f32 v[98:99], v[132:133], v[72:73] op_sel_hi:[0,1]
	v_pk_mul_f32 v[102:103], v[132:133], v[72:73] op_sel:[1,0]
	v_pk_fma_f32 v[94:95], v[132:133], v[60:61], v[94:95] op_sel_hi:[0,1,1]
	v_pk_fma_f32 v[98:99], v[134:135], v[60:61], v[98:99] op_sel_hi:[0,1,1]
	v_pk_fma_f32 v[102:103], v[134:135], v[60:61], v[102:103] op_sel:[1,0,0]
	v_pk_fma_f32 v[94:95], v[132:133], v[64:65], v[94:95] op_sel:[1,0,0]
	v_pk_fma_f32 v[98:99], v[134:135], v[64:65], v[98:99] op_sel:[1,0,0]
	v_pk_fma_f32 v[102:103], v[136:137], v[64:65], v[102:103] op_sel_hi:[0,1,1]
	v_pk_mul_f32 v[68:69], v[128:129], v[94:95] op_sel_hi:[0,1]
	v_pk_fma_f32 v[68:69], v[128:129], v[98:99], v[68:69] op_sel:[1,0,0]
	v_pk_fma_f32 v[68:69], v[130:131], v[102:103], v[68:69] op_sel_hi:[0,1,1]
	v_pk_fma_f32 v[68:69], v[136:137], v[66:67], v[68:69] op_sel:[1,0,0] neg_lo:[0,0,1] neg_hi:[0,0,1]
	s_waitcnt vmcnt(8)
	v_mov_b32_dpp v8, v76 wave_shr:1 row_mask:0xf bank_mask:0xf bound_ctrl:1
	v_mov_b32_dpp v9, v77 wave_shr:1 row_mask:0xf bank_mask:0xf bound_ctrl:1
	v_mov_b32_dpp v10, v78 wave_shr:1 row_mask:0xf bank_mask:0xf bound_ctrl:1
	v_mov_b32_dpp v40, v76 wave_shl:1 row_mask:0xf bank_mask:0xf bound_ctrl:1
	v_mov_b32_dpp v41, v77 wave_shl:1 row_mask:0xf bank_mask:0xf bound_ctrl:1
	v_mov_b32_dpp v42, v78 wave_shl:1 row_mask:0xf bank_mask:0xf bound_ctrl:1
	v_pk_add_f32 v[4:5], v[76:77], v[8:9]
	v_pk_mul_f32 v[44:45], v[76:77], v[76:77] op_sel_hi:[0,1]
	v_pk_mul_f32 v[46:47], v[76:77], v[78:79] op_sel_hi:[1,0]
	v_mul_f32_e64 v60, v77, v77
	v_mul_f32_e64 v61, v78, v78
	v_add_f32_e64 v64, v78, v10
	v_pk_add_f32 v[4:5], v[4:5], v[40:41]
	v_or3_b32 v29, v57, v58, v59
	v_or3_b32 v29, v29, v56, v37
	s_add_i32 s4, s34, -1
	s_cmpk_lt_u32 s4, 0x1ff
	s_cselect_b64 s[12:13], s[42:43], 0
	v_cmp_ne_u32_e64 s[30:31], 0, v29
	s_and_b64 s[30:31], s[30:31], s[12:13]
	v_cndmask_b32_e64 v29, 0, 1.0, s[30:31]
	v_pk_fma_f32 v[44:45], v[8:9], v[8:9], v[44:45] op_sel_hi:[0,1,1]
	v_pk_fma_f32 v[46:47], v[8:9], v[10:11], v[46:47] op_sel_hi:[1,0,1]
	v_fma_f32 v60, v9, v9, v60
	v_fma_f32 v61, v10, v10, v61
	v_add_f32_dpp v65, v29, v29 wave_shr:1 row_mask:0xf bank_mask:0xf bound_ctrl:1
	v_add_f32_e64 v64, v64, v42
	v_pk_fma_f32 v[44:45], v[40:41], v[40:41], v[44:45] op_sel_hi:[0,1,1]
	v_pk_fma_f32 v[46:47], v[40:41], v[42:43], v[46:47] op_sel_hi:[1,0,1]
	v_fma_f32 v60, v41, v41, v60
	v_fma_f32 v61, v42, v42, v61
	v_add_f32_dpp v65, v29, v65 wave_shl:1 row_mask:0xf bank_mask:0xf bound_ctrl:1
	v_pk_add_f32 v[66:67], v[124:125], v[4:5]
	v_pk_add_f32 v[72:73], v[38:39], v[44:45]
	v_pk_add_f32 v[38:39], v[48:49], v[46:47]
	v_pk_add_f32 v[48:49], v[50:51], v[60:61]
	v_pk_add_f32 v[50:51], v[52:53], v[64:65]
	v_mul_f32_e64 v124, v66, v22
	v_mul_f32_e64 v125, v67, v22
	v_mul_f32_e64 v126, v50, v22
	v_fma_f32 v29, v72, v22, v26
	v_mul_f32_e64 v36, v73, v22
	v_mul_f32_e64 v52, v38, v22
	v_fma_f32 v53, v48, v22, v26
	v_mul_f32_e64 v122, v39, v22
	v_fma_f32 v123, v49, v22, v26
	v_fma_f32 v29, -v124, v124, v29
	v_fma_f32 v36, -v124, v125, v36
	v_fma_f32 v52, -v124, v126, v52
	v_fma_f32 v53, -v125, v125, v53
	v_fma_f32 v122, -v125, v126, v122
	v_fma_f32 v123, -v126, v126, v123
	v_mul_f32_e64 v136, v122, v122
	v_mul_f32_e64 v137, v36, v123
	v_mul_f32_e64 v138, v52, v53
	v_mul_f32_e64 v139, v52, v52
	v_mul_f32_e64 v142, v29, v122
	v_mul_f32_e64 v143, v36, v36
	v_fma_f32 v136, v53, v123, -v136
	v_fma_f32 v137, v52, v122, -v137
	v_fma_f32 v138, v36, v122, -v138
	v_fma_f32 v139, v29, v123, -v139
	v_fma_f32 v142, v36, v52, -v142
	v_fma_f32 v143, v29, v53, -v143
	v_mul_f32_e64 v146, v29, v136
	v_fma_f32 v146, v36, v137, v146
	v_fma_f32 v146, v52, v138, v146
	v_rcp_f32_e32 v146, v146
	v_cmp_ne_u32_e64 vcc, s37, v3
	v_mul_f32_e64 v146, v146, v22
	v_cndmask_b32_e64 v146, 0, v146, s[30:31]
	v_cndmask_b32_e64 v29, 0, v18, vcc
	v_cndmask_b32_e64 v133, 0, v22, s[30:31]
	v_mul_f32_e64 v127, v136, v146
	v_mul_f32_e64 v128, v137, v146
	v_mul_f32_e64 v129, v138, v146
	v_mul_f32_e64 v130, v139, v146
	v_mul_f32_e64 v131, v142, v146
	v_mul_f32_e64 v132, v143, v146
	v_add_f32_e64 v134, v51, v29
	v_mov_b32_e32 v135, v3
	ds_write_b128 v23, v[124:127] offset:3072
	ds_write_b128 v23, v[128:131] offset:4096
	ds_write_b128 v23, v[132:135] offset:5120
	v_mov_b32_dpp v36, v30 wave_shr:1 row_mask:0xf bank_mask:0xf bound_ctrl:1
	v_mov_b32_dpp v37, v31 wave_shr:1 row_mask:0xf bank_mask:0xf bound_ctrl:1
	v_mov_b32_dpp v48, v30 wave_shl:1 row_mask:0xf bank_mask:0xf bound_ctrl:1
	v_mov_b32_dpp v49, v31 wave_shl:1 row_mask:0xf bank_mask:0xf bound_ctrl:1
	v_pk_mul_f32 v[38:39], v[30:31], v[76:77] op_sel_hi:[1,0]
	v_pk_mul_f32 v[50:51], v[30:31], v[76:77] op_sel:[0,1]
	v_pk_mul_f32 v[66:67], v[30:31], v[78:79] op_sel_hi:[1,0]
	v_pk_add_f32 v[122:123], v[30:31], v[36:37]
	v_pk_fma_f32 v[38:39], v[36:37], v[8:9], v[38:39] op_sel_hi:[1,0,1]
	v_pk_fma_f32 v[50:51], v[36:37], v[8:9], v[50:51] op_sel:[0,1,0]
	v_pk_fma_f32 v[66:67], v[36:37], v[10:11], v[66:67] op_sel_hi:[1,0,1]
	v_pk_add_f32 v[122:123], v[122:123], v[48:49]
	v_pk_fma_f32 v[38:39], v[48:49], v[40:41], v[38:39] op_sel_hi:[1,0,1]
	v_pk_fma_f32 v[50:51], v[48:49], v[40:41], v[50:51] op_sel:[0,1,0]
	v_pk_fma_f32 v[66:67], v[48:49], v[42:43], v[66:67] op_sel_hi:[1,0,1]
	s_waitcnt lgkmcnt(0)
	s_barrier
	s_add_i32 s5, s34, 4
	s_min_i32 s5, s5, 0x200
	s_mul_i32 s6, s5, 0x804
	s_add_i32 s6, s6, s35
	s_add_i32 s7, s6, 0x505014
	s_add_i32 s8, s6, 0x606018
	s_mul_i32 s9, s5, 0x180c
	s_add_i32 s9, s9, s33
	s_add_i32 s4, s34, 5
	s_min_i32 s4, s4, 0x200
	s_mul_i32 s4, s4, 0x804
	s_add_i32 s4, s4, s38
	buffer_load_dword v3, v28, s[20:23], s4 offen nt
	buffer_load_dwordx3 v[136:138], v27, s[24:27], s9 offen nt
	buffer_load_dword v36, v28, s[16:19], s7 offen nt
	buffer_load_dword v37, v28, s[16:19], s8 offen nt
	s_waitcnt vmcnt(8)
	s_add_i32 s4, s34, 3
	s_cmpk_lt_u32 s4, 0x201
	s_cselect_b64 s[12:13], s[40:41], 0
	v_cmp_eq_u32_e64 s[14:15], s37, v24
	s_and_b64 s[14:15], s[14:15], s[12:13]
	v_cndmask_b32_e64 v29, 0, 1, s[14:15]
	s_nop 1
	v_or_b32_dpp v48, v29, v29 wave_shr:1 row_mask:0xf bank_mask:0xf bound_ctrl:1
	s_nop 1
	v_or_b32_dpp v48, v29, v48 wave_shl:1 row_mask:0xf bank_mask:0xf bound_ctrl:1
	s_nop 1
	v_or_b32_dpp v49, v48, v48 wave_shr:1 row_mask:0xf bank_mask:0xf bound_ctrl:1
	s_nop 1
	v_or_b32_dpp v49, v48, v49 wave_shl:1 row_mask:0xf bank_mask:0xf bound_ctrl:1
	v_pk_add_f32 v[52:53], v[62:63], v[122:123]
	v_pk_add_f32 v[62:63], v[70:71], v[38:39]
	v_pk_add_f32 v[70:71], v[74:75], v[50:51]
	v_pk_add_f32 v[74:75], v[90:91], v[66:67]
	v_pk_fma_f32 v[62:63], v[124:125], v[52:53], v[62:63] op_sel_hi:[0,1,1] neg_lo:[1,0,0] neg_hi:[1,0,0]
	v_pk_fma_f32 v[70:71], v[124:125], v[52:53], v[70:71] op_sel:[1,0,0] neg_lo:[1,0,0] neg_hi:[1,0,0]
	v_pk_fma_f32 v[74:75], v[126:127], v[52:53], v[74:75] op_sel_hi:[0,1,1] neg_lo:[1,0,0] neg_hi:[1,0,0]
	v_pk_mul_f32 v[72:73], v[126:127], v[62:63] op_sel:[1,0]
	v_pk_mul_f32 v[156:157], v[128:129], v[62:63] op_sel_hi:[0,1]
	v_pk_mul_f32 v[160:161], v[128:129], v[62:63] op_sel:[1,0]
	v_pk_fma_f32 v[72:73], v[128:129], v[70:71], v[72:73] op_sel_hi:[0,1,1]
	v_pk_fma_f32 v[156:157], v[130:131], v[70:71], v[156:157] op_sel_hi:[0,1,1]
	v_pk_fma_f32 v[160:161], v[130:131], v[70:71], v[160:161] op_sel:[1,0,0]
	v_pk_fma_f32 v[72:73], v[128:129], v[74:75], v[72:73] op_sel:[1,0,0]
	v_pk_fma_f32 v[156:157], v[130:131], v[74:75], v[156:157] op_sel:[1,0,0]
	v_pk_fma_f32 v[160:161], v[132:133], v[74:75], v[160:161] op_sel_hi:[0,1,1]
	v_pk_mul_f32 v[90:91], v[124:125], v[72:73] op_sel_hi:[0,1]
	v_pk_fma_f32 v[90:91], v[124:125], v[156:157], v[90:91] op_sel:[1,0,0]
	v_pk_fma_f32 v[90:91], v[126:127], v[160:161], v[90:91] op_sel_hi:[0,1,1]
	v_pk_fma_f32 v[90:91], v[132:133], v[52:53], v[90:91] op_sel:[1,0,0] neg_lo:[0,0,1] neg_hi:[0,0,1]
	s_waitcnt vmcnt(8)
	v_mov_b32_dpp v12, v104 wave_shr:1 row_mask:0xf bank_mask:0xf bound_ctrl:1
	v_mov_b32_dpp v13, v105 wave_shr:1 row_mask:0xf bank_mask:0xf bound_ctrl:1
	v_mov_b32_dpp v14, v106 wave_shr:1 row_mask:0xf bank_mask:0xf bound_ctrl:1
	v_mov_b32_dpp v80, v104 wave_shl:1 row_mask:0xf bank_mask:0xf bound_ctrl:1
	v_mov_b32_dpp v81, v105 wave_shl:1 row_mask:0xf bank_mask:0xf bound_ctrl:1
	v_mov_b32_dpp v82, v106 wave_shl:1 row_mask:0xf bank_mask:0xf bound_ctrl:1
	v_pk_add_f32 v[6:7], v[104:105], v[12:13]
	v_pk_mul_f32 v[52:53], v[104:105], v[104:105] op_sel_hi:[0,1]
	v_pk_mul_f32 v[62:63], v[104:105], v[106:107] op_sel_hi:[1,0]
	v_mul_f32_e64 v70, v105, v105
	v_mul_f32_e64 v71, v106, v106
	v_add_f32_e64 v74, v106, v14
	v_pk_add_f32 v[6:7], v[6:7], v[80:81]
	v_or3_b32 v29, v49, v57, v58
	v_or3_b32 v29, v29, v59, v56
	s_add_i32 s4, s34, 0
	s_cmpk_lt_u32 s4, 0x1ff
	s_cselect_b64 s[12:13], s[42:43], 0
	v_cmp_ne_u32_e64 s[30:31], 0, v29
	s_and_b64 s[30:31], s[30:31], s[12:13]
	v_cndmask_b32_e64 v29, 0, 1.0, s[30:31]
	v_pk_fma_f32 v[52:53], v[12:13], v[12:13], v[52:53] op_sel_hi:[0,1,1]
	v_pk_fma_f32 v[62:63], v[12:13], v[14:15], v[62:63] op_sel_hi:[1,0,1]
	v_fma_f32 v70, v13, v13, v70
	v_fma_f32 v71, v14, v14, v71
	v_add_f32_dpp v75, v29, v29 wave_shr:1 row_mask:0xf bank_mask:0xf bound_ctrl:1
	v_add_f32_e64 v74, v74, v82
	v_pk_fma_f32 v[52:53], v[80:81], v[80:81], v[52:53] op_sel_hi:[0,1,1]
	v_pk_fma_f32 v[62:63], v[80:81], v[82:83], v[62:63] op_sel_hi:[1,0,1]
	v_fma_f32 v70, v81, v81, v70
	v_fma_f32 v71, v82, v82, v71
	v_add_f32_dpp v75, v29, v75 wave_shl:1 row_mask:0xf bank_mask:0xf bound_ctrl:1
	v_pk_add_f32 v[86:87], v[4:5], v[6:7]
	v_pk_add_f32 v[84:85], v[96:97], v[86:87]
	v_pk_add_f32 v[126:127], v[44:45], v[52:53]
	v_pk_add_f32 v[4:5], v[100:101], v[126:127]
	v_pk_add_f32 v[130:131], v[46:47], v[62:63]
	v_pk_add_f32 v[44:45], v[116:117], v[130:131]
	v_pk_add_f32 v[96:97], v[60:61], v[70:71]
	v_pk_add_f32 v[46:47], v[118:119], v[96:97]
	v_pk_add_f32 v[118:119], v[64:65], v[74:75]
	v_pk_add_f32 v[60:61], v[120:121], v[118:119]
	v_mul_f32_e64 v132, v84, v22
	v_mul_f32_e64 v133, v85, v22
	v_mul_f32_e64 v134, v60, v22
	v_fma_f32 v29, v4, v22, v26
	v_mul_f32_e64 v48, v5, v22
	v_mul_f32_e64 v64, v44, v22
	v_fma_f32 v65, v46, v22, v26
	v_mul_f32_e64 v100, v45, v22
	v_fma_f32 v101, v47, v22, v26
	v_fma_f32 v29, -v132, v132, v29
	v_fma_f32 v48, -v132, v133, v48
	v_fma_f32 v64, -v132, v134, v64
	v_fma_f32 v65, -v133, v133, v65
	v_fma_f32 v100, -v133, v134, v100
	v_fma_f32 v101, -v134, v134, v101
	v_mul_f32_e64 v116, v100, v100
	v_mul_f32_e64 v117, v48, v101
	v_mul_f32_e64 v120, v64, v65
	v_mul_f32_e64 v121, v64, v64
	v_mul_f32_e64 v124, v29, v100
	v_mul_f32_e64 v125, v48, v48
	v_fma_f32 v116, v65, v101, -v116
	v_fma_f32 v117, v64, v100, -v117
	v_fma_f32 v120, v48, v100, -v120
	v_fma_f32 v121, v29, v101, -v121
	v_fma_f32 v124, v48, v64, -v124
	v_fma_f32 v125, v29, v65, -v125
	v_mul_f32_e64 v128, v29, v116
	v_fma_f32 v128, v48, v117, v128
	v_fma_f32 v128, v64, v120, v128
	v_rcp_f32_e32 v128, v128
	v_cmp_ne_u32_e64 vcc, s37, v16
	v_mul_f32_e64 v128, v128, v22
	v_cndmask_b32_e64 v128, 0, v128, s[30:31]
	v_cndmask_b32_e64 v29, 0, v18, vcc
	v_cndmask_b32_e64 v169, 0, v22, s[30:31]
	v_mul_f32_e64 v135, v116, v128
	v_mul_f32_e64 v164, v117, v128
	v_mul_f32_e64 v165, v120, v128
	v_mul_f32_e64 v166, v121, v128
	v_mul_f32_e64 v167, v124, v128
	v_mul_f32_e64 v168, v125, v128
	v_add_f32_e64 v170, v61, v29
	v_mov_b32_e32 v171, v16
	ds_write_b128 v23, v[132:135]
	ds_write_b128 v23, v[164:167] offset:1024
	ds_write_b128 v23, v[168:171] offset:2048
	v_mov_b32_dpp v46, v92 wave_shr:1 row_mask:0xf bank_mask:0xf bound_ctrl:1
	v_mov_b32_dpp v47, v93 wave_shr:1 row_mask:0xf bank_mask:0xf bound_ctrl:1
	v_mov_b32_dpp v142, v92 wave_shl:1 row_mask:0xf bank_mask:0xf bound_ctrl:1
	v_mov_b32_dpp v143, v93 wave_shl:1 row_mask:0xf bank_mask:0xf bound_ctrl:1
	v_pk_mul_f32 v[4:5], v[92:93], v[104:105] op_sel_hi:[1,0]
	v_pk_mul_f32 v[44:45], v[92:93], v[104:105] op_sel:[0,1]
	v_pk_mul_f32 v[60:61], v[92:93], v[106:107] op_sel_hi:[1,0]
	v_pk_add_f32 v[64:65], v[92:93], v[46:47]
	v_pk_fma_f32 v[4:5], v[46:47], v[12:13], v[4:5] op_sel_hi:[1,0,1]
	v_pk_fma_f32 v[44:45], v[46:47], v[12:13], v[44:45] op_sel:[0,1,0]
	v_pk_fma_f32 v[60:61], v[46:47], v[14:15], v[60:61] op_sel_hi:[1,0,1]
	v_pk_add_f32 v[64:65], v[64:65], v[142:143]
	v_pk_fma_f32 v[4:5], v[142:143], v[80:81], v[4:5] op_sel_hi:[1,0,1]
	v_pk_fma_f32 v[44:45], v[142:143], v[80:81], v[44:45] op_sel:[0,1,0]
	v_pk_fma_f32 v[60:61], v[142:143], v[82:83], v[60:61] op_sel_hi:[1,0,1]
	s_waitcnt lgkmcnt(0)
	s_barrier
	s_add_i32 s5, s34, 5
	s_min_i32 s5, s5, 0x200
	s_mul_i32 s6, s5, 0x804
	s_add_i32 s6, s6, s35
	s_add_i32 s7, s6, 0x505014
	s_add_i32 s8, s6, 0x606018
	s_mul_i32 s9, s5, 0x180c
	s_add_i32 s9, s9, s33
	s_add_i32 s4, s34, 6
	s_min_i32 s4, s4, 0x200
	s_mul_i32 s4, s4, 0x804
	s_add_i32 s4, s4, s38
	buffer_load_dword v16, v28, s[20:23], s4 offen nt
	buffer_load_dwordx3 v[172:174], v27, s[24:27], s9 offen nt
	buffer_load_dword v46, v28, s[16:19], s7 offen nt
	buffer_load_dword v47, v28, s[16:19], s8 offen nt
	s_waitcnt vmcnt(8)
	s_add_i32 s4, s34, 4
	s_cmpk_lt_u32 s4, 0x201
	s_cselect_b64 s[12:13], s[40:41], 0
	v_cmp_eq_u32_e64 s[14:15], s37, v2
	s_and_b64 s[14:15], s[14:15], s[12:13]
	v_cndmask_b32_e64 v29, 0, 1, s[14:15]
	s_nop 1
	v_or_b32_dpp v48, v29, v29 wave_shr:1 row_mask:0xf bank_mask:0xf bound_ctrl:1
	s_nop 1
	v_or_b32_dpp v48, v29, v48 wave_shl:1 row_mask:0xf bank_mask:0xf bound_ctrl:1
	s_nop 1
	v_or_b32_dpp v56, v48, v48 wave_shr:1 row_mask:0xf bank_mask:0xf bound_ctrl:1
	s_nop 1
	v_or_b32_dpp v56, v48, v56 wave_shl:1 row_mask:0xf bank_mask:0xf bound_ctrl:1
	v_pk_add_f32 v[142:143], v[122:123], v[64:65]
	v_pk_add_f32 v[84:85], v[148:149], v[142:143]
	v_pk_add_f32 v[122:123], v[38:39], v[4:5]
	v_pk_add_f32 v[146:147], v[88:89], v[122:123]
	v_pk_add_f32 v[38:39], v[50:51], v[44:45]
	v_pk_add_f32 v[150:151], v[140:141], v[38:39]
	v_pk_add_f32 v[50:51], v[66:67], v[60:61]
	v_pk_add_f32 v[158:159], v[144:145], v[50:51]
	v_pk_fma_f32 v[146:147], v[132:133], v[84:85], v[146:147] op_sel_hi:[0,1,1] neg_lo:[1,0,0] neg_hi:[1,0,0]
	v_pk_fma_f32 v[150:151], v[132:133], v[84:85], v[150:151] op_sel:[1,0,0] neg_lo:[1,0,0] neg_hi:[1,0,0]
	v_pk_fma_f32 v[158:159], v[134:135], v[84:85], v[158:159] op_sel_hi:[0,1,1] neg_lo:[1,0,0] neg_hi:[1,0,0]
	v_pk_mul_f32 v[88:89], v[134:135], v[146:147] op_sel:[1,0]
	v_pk_mul_f32 v[100:101], v[164:165], v[146:147] op_sel_hi:[0,1]
	v_pk_mul_f32 v[116:117], v[164:165], v[146:147] op_sel:[1,0]
	v_pk_fma_f32 v[88:89], v[164:165], v[150:151], v[88:89] op_sel_hi:[0,1,1]
	v_pk_fma_f32 v[100:101], v[166:167], v[150:151], v[100:101] op_sel_hi:[0,1,1]
	v_pk_fma_f32 v[116:117], v[166:167], v[150:151], v[116:117] op_sel:[1,0,0]
	v_pk_fma_f32 v[88:89], v[164:165], v[158:159], v[88:89] op_sel:[1,0,0]
	v_pk_fma_f32 v[100:101], v[166:167], v[158:159], v[100:101] op_sel:[1,0,0]
	v_pk_fma_f32 v[116:117], v[168:169], v[158:159], v[116:117] op_sel_hi:[0,1,1]
	v_pk_mul_f32 v[66:67], v[132:133], v[88:89] op_sel_hi:[0,1]
	v_pk_fma_f32 v[66:67], v[132:133], v[100:101], v[66:67] op_sel:[1,0,0]
	v_pk_fma_f32 v[66:67], v[134:135], v[116:117], v[66:67] op_sel_hi:[0,1,1]
	v_pk_fma_f32 v[66:67], v[168:169], v[84:85], v[66:67] op_sel:[1,0,0] neg_lo:[0,0,1] neg_hi:[0,0,1]
	v_cmp_eq_u32_e64 s[10:11], 6, v171
	v_cmp_eq_u32_e64 s[14:15], 7, v171
	v_pk_add_f32 v[84:85], v[72:73], v[88:89]
	v_pk_add_f32 v[120:121], v[94:95], v[84:85]
	v_pk_add_f32 v[72:73], v[156:157], v[100:101]
	v_pk_add_f32 v[94:95], v[98:99], v[72:73]
	v_pk_add_f32 v[124:125], v[160:161], v[116:117]
	v_pk_add_f32 v[98:99], v[102:103], v[124:125]
	v_pk_add_f32 v[102:103], v[90:91], v[66:67]
	v_pk_add_f32 v[128:129], v[68:69], v[102:103]
	v_pk_fma_f32 v[68:69], v[108:109], v[120:121], v[128:129] op_sel_hi:[0,1,1]
	v_pk_fma_f32 v[140:141], v[112:113], v[120:121], v[128:129] op_sel_hi:[0,1,1]
	v_pk_fma_f32 v[68:69], v[108:109], v[94:95], v[68:69] op_sel:[1,0,0]
	v_pk_fma_f32 v[140:141], v[112:113], v[94:95], v[140:141] op_sel:[1,0,0]
	v_pk_fma_f32 v[68:69], v[110:111], v[98:99], v[68:69] op_sel_hi:[0,1,1]
	v_pk_fma_f32 v[140:141], v[114:115], v[98:99], v[140:141] op_sel_hi:[0,1,1]
	v_pk_fma_f32 v[128:129], v[32:33], v[120:121], v[128:129] op_sel_hi:[0,1,1]
	v_pk_fma_f32 v[128:129], v[32:33], v[94:95], v[128:129] op_sel:[1,0,0]
	v_pk_fma_f32 v[128:129], v[34:35], v[98:99], v[128:129] op_sel_hi:[0,1,1]
	v_cndmask_b32_e64 v90, 0, v18, s[10:11]
	v_cndmask_b32_e64 v91, 0, v18, s[14:15]
	v_add_f32_dpp v128, v68, v128 wave_shl:1 row_mask:0xf bank_mask:0xf bound_ctrl:1
	v_add_f32_dpp v129, v69, v129 wave_shl:1 row_mask:0xf bank_mask:0xf bound_ctrl:1
	s_add_i32 s4, s34, 0
	s_cmpk_lt_i32 s4, 0x201
	s_cselect_b64 s[12:13], s[0:1], 0
	v_add_f32_dpp v128, v140, v128 wave_shr:1 row_mask:0xf bank_mask:0xf bound_ctrl:1
	v_add_f32_dpp v129, v141, v129 wave_shr:1 row_mask:0xf bank_mask:0xf bound_ctrl:1
	v_pk_fma_f32 v[128:129], v[20:21], v[170:171], v[128:129] op_sel_hi:[1,0,1] neg_lo:[0,0,1] neg_hi:[0,0,1]
	v_pk_add_f32 v[128:129], v[128:129], v[90:91] neg_lo:[0,1] neg_hi:[0,1]
	v_pk_mul_f32 v[144:145], v[128:129], v[128:129]
	v_add_f32_e32 v144, v144, v145
	v_cndmask_b32_e64 v145, 0, v144, s[12:13]
	v_add_f32_e32 v1, v1, v145
	s_waitcnt vmcnt(8)
	v_mov_b32_dpp v32, v152 wave_shr:1 row_mask:0xf bank_mask:0xf bound_ctrl:1
	v_mov_b32_dpp v33, v153 wave_shr:1 row_mask:0xf bank_mask:0xf bound_ctrl:1
	v_mov_b32_dpp v34, v154 wave_shr:1 row_mask:0xf bank_mask:0xf bound_ctrl:1
	v_mov_b32_dpp v108, v152 wave_shl:1 row_mask:0xf bank_mask:0xf bound_ctrl:1
	v_mov_b32_dpp v109, v153 wave_shl:1 row_mask:0xf bank_mask:0xf bound_ctrl:1
	v_mov_b32_dpp v110, v154 wave_shl:1 row_mask:0xf bank_mask:0xf bound_ctrl:1
	v_pk_add_f32 v[20:21], v[152:153], v[32:33]
	v_pk_mul_f32 v[68:69], v[152:153], v[152:153] op_sel_hi:[0,1]
	v_pk_mul_f32 v[90:91], v[152:153], v[154:155] op_sel_hi:[1,0]
	v_mul_f32_e64 v94, v153, v153
	v_mul_f32_e64 v95, v154, v154
	v_add_f32_e64 v98, v154, v34
	v_pk_add_f32 v[20:21], v[20:21], v[108:109]
	v_or3_b32 v29, v56, v49, v57
	v_or3_b32 v29, v29, v58, v59
	s_add_i32 s4, s34, 1
	s_cmpk_lt_u32 s4, 0x1ff
	s_cselect_b64 s[12:13], s[42:43], 0
	v_cmp_ne_u32_e64 s[30:31], 0, v29
	s_and_b64 s[30:31], s[30:31], s[12:13]
	v_cndmask_b32_e64 v29, 0, 1.0, s[30:31]
	v_pk_fma_f32 v[68:69], v[32:33], v[32:33], v[68:69] op_sel_hi:[0,1,1]
	v_pk_fma_f32 v[90:91], v[32:33], v[34:35], v[90:91] op_sel_hi:[1,0,1]
	v_fma_f32 v94, v33, v33, v94
	v_fma_f32 v95, v34, v34, v95
	v_add_f32_dpp v99, v29, v29 wave_shr:1 row_mask:0xf bank_mask:0xf bound_ctrl:1
	v_add_f32_e64 v98, v98, v110
	v_pk_fma_f32 v[68:69], v[108:109], v[108:109], v[68:69] op_sel_hi:[0,1,1]
	v_pk_fma_f32 v[90:91], v[108:109], v[110:111], v[90:91] op_sel_hi:[1,0,1]
	v_fma_f32 v94, v109, v109, v94
	v_fma_f32 v95, v110, v110, v95
	v_add_f32_dpp v99, v29, v99 wave_shl:1 row_mask:0xf bank_mask:0xf bound_ctrl:1
	v_pk_add_f32 v[112:113], v[86:87], v[20:21]
	v_pk_add_f32 v[86:87], v[126:127], v[68:69]
	v_pk_add_f32 v[114:115], v[130:131], v[90:91]
	v_pk_add_f32 v[120:121], v[96:97], v[94:95]
	v_pk_add_f32 v[96:97], v[118:119], v[98:99]
	v_mul_f32_e64 v128, v112, v22
	v_mul_f32_e64 v129, v113, v22
	v_mul_f32_e64 v130, v96, v22
	v_fma_f32 v29, v86, v22, v26
	v_mul_f32_e64 v48, v87, v22
	v_mul_f32_e64 v118, v114, v22
	v_fma_f32 v119, v120, v22, v26
	v_mul_f32_e64 v126, v115, v22
	v_fma_f32 v127, v121, v22, v26
	v_fma_f32 v29, -v128, v128, v29
	v_fma_f32 v48, -v128, v129, v48
	v_fma_f32 v118, -v128, v130, v118
	v_fma_f32 v119, -v129, v129, v119
	v_fma_f32 v126, -v129, v130, v126
	v_fma_f32 v127, -v130, v130, v127
	v_mul_f32_e64 v140, v126, v126
	v_mul_f32_e64 v141, v48, v127
	v_mul_f32_e64 v148, v118, v119
	v_mul_f32_e64 v149, v118, v118
	v_mul_f32_e64 v150, v29, v126
	v_mul_f32_e64 v151, v48, v48
	v_fma_f32 v140, v119, v127, -v140
	v_fma_f32 v141, v118, v126, -v141
	v_fma_f32 v148, v48, v126, -v148
	v_fma_f32 v149, v29, v127, -v149
	v_fma_f32 v150, v48, v118, -v150
	v_fma_f32 v151, v29, v119, -v151
	v_mul_f32_e64 v156, v29, v140
	v_fma_f32 v156, v48, v141, v156
	v_fma_f32 v156, v118, v148, v156
	v_rcp_f32_e32 v156, v156
	v_cmp_ne_u32_e64 vcc, s37, v17
	v_mul_f32_e64 v156, v156, v22
	v_cndmask_b32_e64 v156, 0, v156, s[30:31]
	v_cndmask_b32_e64 v29, 0, v18, vcc
	v_cndmask_b32_e64 v145, 0, v22, s[30:31]
	v_mul_f32_e64 v131, v140, v156
	v_mul_f32_e64 v132, v141, v156
	v_mul_f32_e64 v133, v148, v156
	v_mul_f32_e64 v134, v149, v156
	v_mul_f32_e64 v135, v150, v156
	v_mul_f32_e64 v144, v151, v156
	v_add_f32_e64 v146, v97, v29
	v_mov_b32_e32 v147, v17
	ds_write_b128 v23, v[128:131] offset:3072
	ds_write_b128 v23, v[132:135] offset:4096
	ds_write_b128 v23, v[144:147] offset:5120
	v_mov_b32_dpp v96, v54 wave_shr:1 row_mask:0xf bank_mask:0xf bound_ctrl:1
	v_mov_b32_dpp v97, v55 wave_shr:1 row_mask:0xf bank_mask:0xf bound_ctrl:1
	v_mov_b32_dpp v112, v54 wave_shl:1 row_mask:0xf bank_mask:0xf bound_ctrl:1
	v_mov_b32_dpp v113, v55 wave_shl:1 row_mask:0xf bank_mask:0xf bound_ctrl:1
	v_pk_mul_f32 v[86:87], v[54:55], v[152:153] op_sel_hi:[1,0]
	v_pk_mul_f32 v[114:115], v[54:55], v[152:153] op_sel:[0,1]
	v_pk_mul_f32 v[118:119], v[54:55], v[154:155] op_sel_hi:[1,0]
	v_pk_add_f32 v[126:127], v[54:55], v[96:97]
	v_pk_fma_f32 v[86:87], v[96:97], v[32:33], v[86:87] op_sel_hi:[1,0,1]
	v_pk_fma_f32 v[114:115], v[96:97], v[32:33], v[114:115] op_sel:[0,1,0]
	v_pk_fma_f32 v[118:119], v[96:97], v[34:35], v[118:119] op_sel_hi:[1,0,1]
	v_pk_add_f32 v[126:127], v[126:127], v[112:113]
	v_pk_fma_f32 v[86:87], v[112:113], v[108:109], v[86:87] op_sel_hi:[1,0,1]
	v_pk_fma_f32 v[114:115], v[112:113], v[108:109], v[114:115] op_sel:[0,1,0]
	v_pk_fma_f32 v[118:119], v[112:113], v[110:111], v[118:119] op_sel_hi:[1,0,1]
	s_waitcnt lgkmcnt(0)
	s_barrier
	s_add_i32 s5, s34, 6
	s_min_i32 s5, s5, 0x200
	s_mul_i32 s6, s5, 0x804
	s_add_i32 s6, s6, s35
	s_add_i32 s7, s6, 0x505014
	s_add_i32 s8, s6, 0x606018
	s_mul_i32 s9, s5, 0x180c
	s_add_i32 s9, s9, s33
	s_add_i32 s4, s34, 7
	s_min_i32 s4, s4, 0x200
	s_mul_i32 s4, s4, 0x804
	s_add_i32 s4, s4, s38
	buffer_load_dword v17, v28, s[20:23], s4 offen nt
	buffer_load_dwordx3 v[148:150], v27, s[24:27], s9 offen nt
	buffer_load_dword v96, v28, s[16:19], s7 offen nt
	buffer_load_dword v97, v28, s[16:19], s8 offen nt
	s_waitcnt vmcnt(8)
	s_add_i32 s4, s34, 5
	s_cmpk_lt_u32 s4, 0x201
	s_cselect_b64 s[12:13], s[40:41], 0
	v_cmp_eq_u32_e64 s[14:15], s37, v3
	s_and_b64 s[14:15], s[14:15], s[12:13]
	v_cndmask_b32_e64 v29, 0, 1, s[14:15]
	s_nop 1
	v_or_b32_dpp v48, v29, v29 wave_shr:1 row_mask:0xf bank_mask:0xf bound_ctrl:1
	s_nop 1
	v_or_b32_dpp v48, v29, v48 wave_shl:1 row_mask:0xf bank_mask:0xf bound_ctrl:1
	s_nop 1
	v_or_b32_dpp v59, v48, v48 wave_shr:1 row_mask:0xf bank_mask:0xf bound_ctrl:1
	s_nop 1
	v_or_b32_dpp v59, v48, v59 wave_shl:1 row_mask:0xf bank_mask:0xf bound_ctrl:1
	v_pk_add_f32 v[112:113], v[142:143], v[126:127]
	v_pk_add_f32 v[142:143], v[122:123], v[86:87]
	v_pk_add_f32 v[122:123], v[38:39], v[114:115]
	v_pk_add_f32 v[38:39], v[50:51], v[118:119]
	v_pk_fma_f32 v[142:143], v[128:129], v[112:113], v[142:143] op_sel_hi:[0,1,1] neg_lo:[1,0,0] neg_hi:[1,0,0]
	v_pk_fma_f32 v[122:123], v[128:129], v[112:113], v[122:123] op_sel:[1,0,0] neg_lo:[1,0,0] neg_hi:[1,0,0]
	v_pk_fma_f32 v[38:39], v[130:131], v[112:113], v[38:39] op_sel_hi:[0,1,1] neg_lo:[1,0,0] neg_hi:[1,0,0]
	v_pk_mul_f32 v[120:121], v[130:131], v[142:143] op_sel:[1,0]
	v_pk_mul_f32 v[140:141], v[132:133], v[142:143] op_sel_hi:[0,1]
	v_pk_mul_f32 v[156:157], v[132:133], v[142:143] op_sel:[1,0]
	v_pk_fma_f32 v[120:121], v[132:133], v[122:123], v[120:121] op_sel_hi:[0,1,1]
	v_pk_fma_f32 v[140:141], v[134:135], v[122:123], v[140:141] op_sel_hi:[0,1,1]
	v_pk_fma_f32 v[156:157], v[134:135], v[122:123], v[156:157] op_sel:[1,0,0]
	v_pk_fma_f32 v[120:121], v[132:133], v[38:39], v[120:121] op_sel:[1,0,0]
	v_pk_fma_f32 v[140:141], v[134:135], v[38:39], v[140:141] op_sel:[1,0,0]
	v_pk_fma_f32 v[156:157], v[144:145], v[38:39], v[156:157] op_sel_hi:[0,1,1]
	v_pk_mul_f32 v[50:51], v[128:129], v[120:121] op_sel_hi:[0,1]
	v_pk_fma_f32 v[50:51], v[128:129], v[140:141], v[50:51] op_sel:[1,0,0]
	v_pk_fma_f32 v[50:51], v[130:131], v[156:157], v[50:51] op_sel_hi:[0,1,1]
	v_pk_fma_f32 v[50:51], v[144:145], v[112:113], v[50:51] op_sel:[1,0,0] neg_lo:[0,0,1] neg_hi:[0,0,1]
	v_cmp_eq_u32_e64 s[10:11], 6, v147
	v_cmp_eq_u32_e64 s[14:15], 7, v147
	v_pk_add_f32 v[38:39], v[84:85], v[120:121]
	v_pk_add_f32 v[84:85], v[72:73], v[140:141]
	v_pk_add_f32 v[72:73], v[124:125], v[156:157]
	v_pk_add_f32 v[122:123], v[102:103], v[50:51]
	v_pk_fma_f32 v[102:103], v[8:9], v[38:39], v[122:123] op_sel_hi:[0,1,1]
	v_pk_fma_f32 v[142:143], v[40:41], v[38:39], v[122:123] op_sel_hi:[0,1,1]
	v_pk_fma_f32 v[102:103], v[8:9], v[84:85], v[102:103] op_sel:[1,0,0]
	v_pk_fma_f32 v[142:143], v[40:41], v[84:85], v[142:143] op_sel:[1,0,0]
	v_pk_fma_f32 v[102:103], v[10:11], v[72:73], v[102:103] op_sel_hi:[0,1,1]
	v_pk_fma_f32 v[142:143], v[42:43], v[72:73], v[142:143] op_sel_hi:[0,1,1]
	v_pk_fma_f32 v[122:123], v[76:77], v[38:39], v[122:123] op_sel_hi:[0,1,1]
	v_pk_fma_f32 v[122:123], v[76:77], v[84:85], v[122:123] op_sel:[1,0,0]
	v_pk_fma_f32 v[122:123], v[78:79], v[72:73], v[122:123] op_sel_hi:[0,1,1]
	v_cndmask_b32_e64 v112, 0, v18, s[10:11]
	v_cndmask_b32_e64 v113, 0, v18, s[14:15]
	v_add_f32_dpp v122, v102, v122 wave_shl:1 row_mask:0xf bank_mask:0xf bound_ctrl:1
	v_add_f32_dpp v123, v103, v123 wave_shl:1 row_mask:0xf bank_mask:0xf bound_ctrl:1
	s_add_i32 s4, s34, 1
	s_cmpk_lt_i32 s4, 0x201
	s_cselect_b64 s[12:13], s[0:1], 0
	v_add_f32_dpp v122, v142, v122 wave_shr:1 row_mask:0xf bank_mask:0xf bound_ctrl:1
	v_add_f32_dpp v123, v143, v123 wave_shr:1 row_mask:0xf bank_mask:0xf bound_ctrl:1
	v_pk_fma_f32 v[122:123], v[30:31], v[146:147], v[122:123] op_sel_hi:[1,0,1] neg_lo:[0,0,1] neg_hi:[0,0,1]
	v_pk_add_f32 v[122:123], v[122:123], v[112:113] neg_lo:[0,1] neg_hi:[0,1]
	v_pk_mul_f32 v[124:125], v[122:123], v[122:123]
	v_add_f32_e32 v124, v124, v125
	v_cndmask_b32_e64 v125, 0, v124, s[12:13]
	v_add_f32_e32 v1, v1, v125
	s_waitcnt vmcnt(8)
	v_mov_b32_dpp v8, v136 wave_shr:1 row_mask:0xf bank_mask:0xf bound_ctrl:1
	v_mov_b32_dpp v9, v137 wave_shr:1 row_mask:0xf bank_mask:0xf bound_ctrl:1
	v_mov_b32_dpp v10, v138 wave_shr:1 row_mask:0xf bank_mask:0xf bound_ctrl:1
	v_mov_b32_dpp v40, v136 wave_shl:1 row_mask:0xf bank_mask:0xf bound_ctrl:1
	v_mov_b32_dpp v41, v137 wave_shl:1 row_mask:0xf bank_mask:0xf bound_ctrl:1
	v_mov_b32_dpp v42, v138 wave_shl:1 row_mask:0xf bank_mask:0xf bound_ctrl:1
	v_pk_add_f32 v[30:31], v[136:137], v[8:9]
	v_pk_mul_f32 v[38:39], v[136:137], v[136:137] op_sel_hi:[0,1]
	v_pk_mul_f32 v[72:73], v[136:137], v[138:139] op_sel_hi:[1,0]
	v_mul_f32_e64 v76, v137, v137
	v_mul_f32_e64 v77, v138, v138
	v_add_f32_e64 v78, v138, v10
	v_pk_add_f32 v[30:31], v[30:31], v[40:41]
	v_or3_b32 v29, v59, v56, v49
	v_or3_b32 v29, v29, v57, v58
	s_add_i32 s4, s34, 2
	s_cmpk_lt_u32 s4, 0x1ff
	s_cselect_b64 s[12:13], s[42:43], 0
	v_cmp_ne_u32_e64 s[30:31], 0, v29
	s_and_b64 s[30:31], s[30:31], s[12:13]
	v_cndmask_b32_e64 v29, 0, 1.0, s[30:31]
	v_pk_fma_f32 v[38:39], v[8:9], v[8:9], v[38:39] op_sel_hi:[0,1,1]
	v_pk_fma_f32 v[72:73], v[8:9], v[10:11], v[72:73] op_sel_hi:[1,0,1]
	v_fma_f32 v76, v9, v9, v76
	v_fma_f32 v77, v10, v10, v77
	v_add_f32_dpp v79, v29, v29 wave_shr:1 row_mask:0xf bank_mask:0xf bound_ctrl:1
	v_add_f32_e64 v78, v78, v42
	v_pk_fma_f32 v[38:39], v[40:41], v[40:41], v[38:39] op_sel_hi:[0,1,1]
	v_pk_fma_f32 v[72:73], v[40:41], v[42:43], v[72:73] op_sel_hi:[1,0,1]
	v_fma_f32 v76, v41, v41, v76
	v_fma_f32 v77, v42, v42, v77
	v_add_f32_dpp v79, v29, v79 wave_shl:1 row_mask:0xf bank_mask:0xf bound_ctrl:1
	v_pk_add_f32 v[84:85], v[20:21], v[30:31]
	v_pk_add_f32 v[102:103], v[6:7], v[84:85]
	v_pk_add_f32 v[6:7], v[68:69], v[38:39]
	v_pk_add_f32 v[20:21], v[52:53], v[6:7]
	v_pk_add_f32 v[52:53], v[90:91], v[72:73]
	v_pk_add_f32 v[68:69], v[62:63], v[52:53]
	v_pk_add_f32 v[112:113], v[94:95], v[76:77]
	v_pk_add_f32 v[62:63], v[70:71], v[112:113]
	v_pk_add_f32 v[124:125], v[98:99], v[78:79]
	v_pk_add_f32 v[70:71], v[74:75], v[124:125]
	v_mul_f32_e64 v128, v102, v22
	v_mul_f32_e64 v129, v103, v22
	v_mul_f32_e64 v130, v70, v22
	v_fma_f32 v29, v20, v22, v26
	v_mul_f32_e64 v48, v21, v22
	v_mul_f32_e64 v74, v68, v22
	v_fma_f32 v75, v62, v22, v26
	v_mul_f32_e64 v90, v69, v22
	v_fma_f32 v91, v63, v22, v26
	v_fma_f32 v29, -v128, v128, v29
	v_fma_f32 v48, -v128, v129, v48
	v_fma_f32 v74, -v128, v130, v74
	v_fma_f32 v75, -v129, v129, v75
	v_fma_f32 v90, -v129, v130, v90
	v_fma_f32 v91, -v130, v130, v91
	v_mul_f32_e64 v94, v90, v90
	v_mul_f32_e64 v95, v48, v91
	v_mul_f32_e64 v98, v74, v75
	v_mul_f32_e64 v99, v74, v74
	v_mul_f32_e64 v122, v29, v90
	v_mul_f32_e64 v123, v48, v48
	v_fma_f32 v94, v75, v91, -v94
	v_fma_f32 v95, v74, v90, -v95
	v_fma_f32 v98, v48, v90, -v98
	v_fma_f32 v99, v29, v91, -v99
	v_fma_f32 v122, v48, v74, -v122
	v_fma_f32 v123, v29, v75, -v123
	v_mul_f32_e64 v142, v29, v94
	v_fma_f32 v142, v48, v95, v142
	v_fma_f32 v142, v74, v98, v142
	v_rcp_f32_e32 v142, v142
	v_cmp_ne_u32_e64 vcc, s37, v25
	v_mul_f32_e64 v142, v142, v22
	v_cndmask_b32_e64 v142, 0, v142, s[30:31]
	v_cndmask_b32_e64 v29, 0, v18, vcc
	v_cndmask_b32_e64 v145, 0, v22, s[30:31]
	v_mul_f32_e64 v131, v94, v142
	v_mul_f32_e64 v132, v95, v142
	v_mul_f32_e64 v133, v98, v142
	v_mul_f32_e64 v134, v99, v142
	v_mul_f32_e64 v135, v122, v142
	v_mul_f32_e64 v144, v123, v142
	v_add_f32_e64 v146, v71, v29
	v_mov_b32_e32 v147, v25
	ds_write_b128 v23, v[128:131]
	ds_write_b128 v23, v[132:135] offset:1024
	ds_write_b128 v23, v[144:147] offset:2048
	v_mov_b32_dpp v62, v36 wave_shr:1 row_mask:0xf bank_mask:0xf bound_ctrl:1
	v_mov_b32_dpp v63, v37 wave_shr:1 row_mask:0xf bank_mask:0xf bound_ctrl:1
	v_mov_b32_dpp v70, v36 wave_shl:1 row_mask:0xf bank_mask:0xf bound_ctrl:1
	v_mov_b32_dpp v71, v37 wave_shl:1 row_mask:0xf bank_mask:0xf bound_ctrl:1
	v_pk_mul_f32 v[20:21], v[36:37], v[136:137] op_sel_hi:[1,0]
	v_pk_mul_f32 v[68:69], v[36:37], v[136:137] op_sel:[0,1]
	v_pk_mul_f32 v[160:161], v[36:37], v[138:139] op_sel_hi:[1,0]
	v_pk_add_f32 v[164:165], v[36:37], v[62:63]
	v_pk_fma_f32 v[20:21], v[62:63], v[8:9], v[20:21] op_sel_hi:[1,0,1]
	v_pk_fma_f32 v[68:69], v[62:63], v[8:9], v[68:69] op_sel:[0,1,0]
	v_pk_fma_f32 v[160:161], v[62:63], v[10:11], v[160:161] op_sel_hi:[1,0,1]
	v_pk_add_f32 v[164:165], v[164:165], v[70:71]
	v_pk_fma_f32 v[20:21], v[70:71], v[40:41], v[20:21] op_sel_hi:[1,0,1]
	v_pk_fma_f32 v[68:69], v[70:71], v[40:41], v[68:69] op_sel:[0,1,0]
	v_pk_fma_f32 v[160:161], v[70:71], v[42:43], v[160:161] op_sel_hi:[1,0,1]
	s_waitcnt lgkmcnt(0)
	s_barrier
	s_add_i32 s5, s34, 7
	s_min_i32 s5, s5, 0x200
	s_mul_i32 s6, s5, 0x804
	s_add_i32 s6, s6, s35
	s_add_i32 s7, s6, 0x505014
	s_add_i32 s8, s6, 0x606018
	s_mul_i32 s9, s5, 0x180c
	s_add_i32 s9, s9, s33
	s_add_i32 s4, s34, 8
	s_min_i32 s4, s4, 0x200
	s_mul_i32 s4, s4, 0x804
	s_add_i32 s4, s4, s38
	buffer_load_dword v25, v28, s[20:23], s4 offen nt
	buffer_load_dwordx3 v[168:170], v27, s[24:27], s9 offen nt
	buffer_load_dword v62, v28, s[16:19], s7 offen nt
	buffer_load_dword v63, v28, s[16:19], s8 offen nt
	s_waitcnt vmcnt(8)
	s_add_i32 s4, s34, 6
	s_cmpk_lt_u32 s4, 0x201
	s_cselect_b64 s[12:13], s[40:41], 0
	v_cmp_eq_u32_e64 s[14:15], s37, v16
	s_and_b64 s[14:15], s[14:15], s[12:13]
	v_cndmask_b32_e64 v29, 0, 1, s[14:15]
	s_nop 1
	v_or_b32_dpp v48, v29, v29 wave_shr:1 row_mask:0xf bank_mask:0xf bound_ctrl:1
	s_nop 1
	v_or_b32_dpp v48, v29, v48 wave_shl:1 row_mask:0xf bank_mask:0xf bound_ctrl:1
	s_nop 1
	v_or_b32_dpp v58, v48, v48 wave_shr:1 row_mask:0xf bank_mask:0xf bound_ctrl:1
	s_nop 1
	v_or_b32_dpp v58, v48, v58 wave_shl:1 row_mask:0xf bank_mask:0xf bound_ctrl:1
	v_pk_add_f32 v[70:71], v[126:127], v[164:165]
	v_pk_add_f32 v[74:75], v[64:65], v[70:71]
	v_pk_add_f32 v[90:91], v[86:87], v[20:21]
	v_pk_add_f32 v[64:65], v[4:5], v[90:91]
	v_pk_add_f32 v[86:87], v[114:115], v[68:69]
	v_pk_add_f32 v[4:5], v[44:45], v[86:87]
	v_pk_add_f32 v[94:95], v[118:119], v[160:161]
	v_pk_add_f32 v[44:45], v[60:61], v[94:95]
	v_pk_fma_f32 v[64:65], v[128:129], v[74:75], v[64:65] op_sel_hi:[0,1,1] neg_lo:[1,0,0] neg_hi:[1,0,0]
	v_pk_fma_f32 v[4:5], v[128:129], v[74:75], v[4:5] op_sel:[1,0,0] neg_lo:[1,0,0] neg_hi:[1,0,0]
	v_pk_fma_f32 v[44:45], v[130:131], v[74:75], v[44:45] op_sel_hi:[0,1,1] neg_lo:[1,0,0] neg_hi:[1,0,0]
	v_pk_mul_f32 v[98:99], v[130:131], v[64:65] op_sel:[1,0]
	v_pk_mul_f32 v[102:103], v[132:133], v[64:65] op_sel_hi:[0,1]
	v_pk_mul_f32 v[114:115], v[132:133], v[64:65] op_sel:[1,0]
	v_pk_fma_f32 v[98:99], v[132:133], v[4:5], v[98:99] op_sel_hi:[0,1,1]
	v_pk_fma_f32 v[102:103], v[134:135], v[4:5], v[102:103] op_sel_hi:[0,1,1]
	v_pk_fma_f32 v[114:115], v[134:135], v[4:5], v[114:115] op_sel:[1,0,0]
	v_pk_fma_f32 v[98:99], v[132:133], v[44:45], v[98:99] op_sel:[1,0,0]
	v_pk_fma_f32 v[102:103], v[134:135], v[44:45], v[102:103] op_sel:[1,0,0]
	v_pk_fma_f32 v[114:115], v[144:145], v[44:45], v[114:115] op_sel_hi:[0,1,1]
	v_pk_mul_f32 v[60:61], v[128:129], v[98:99] op_sel_hi:[0,1]
	v_pk_fma_f32 v[60:61], v[128:129], v[102:103], v[60:61] op_sel:[1,0,0]
	v_pk_fma_f32 v[60:61], v[130:131], v[114:115], v[60:61] op_sel_hi:[0,1,1]
	v_pk_fma_f32 v[60:61], v[144:145], v[74:75], v[60:61] op_sel:[1,0,0] neg_lo:[0,0,1] neg_hi:[0,0,1]
	v_cmp_eq_u32_e64 s[10:11], 6, v147
	v_cmp_eq_u32_e64 s[14:15], 7, v147
	v_pk_add_f32 v[74:75], v[120:121], v[98:99]
	v_pk_add_f32 v[4:5], v[88:89], v[74:75]
	v_pk_add_f32 v[118:119], v[140:141], v[102:103]
	v_pk_add_f32 v[44:45], v[100:101], v[118:119]
	v_pk_add_f32 v[122:123], v[156:157], v[114:115]
	v_pk_add_f32 v[64:65], v[116:117], v[122:123]
	v_pk_add_f32 v[88:89], v[50:51], v[60:61]
	v_pk_add_f32 v[126:127], v[66:67], v[88:89]
	v_pk_fma_f32 v[50:51], v[12:13], v[4:5], v[126:127] op_sel_hi:[0,1,1]
	v_pk_fma_f32 v[66:67], v[80:81], v[4:5], v[126:127] op_sel_hi:[0,1,1]
	v_pk_fma_f32 v[50:51], v[12:13], v[44:45], v[50:51] op_sel:[1,0,0]
	v_pk_fma_f32 v[66:67], v[80:81], v[44:45], v[66:67] op_sel:[1,0,0]
	v_pk_fma_f32 v[50:51], v[14:15], v[64:65], v[50:51] op_sel_hi:[0,1,1]
	v_pk_fma_f32 v[66:67], v[82:83], v[64:65], v[66:67] op_sel_hi:[0,1,1]
	v_pk_fma_f32 v[126:127], v[104:105], v[4:5], v[126:127] op_sel_hi:[0,1,1]
	v_pk_fma_f32 v[126:127], v[104:105], v[44:45], v[126:127] op_sel:[1,0,0]
	v_pk_fma_f32 v[126:127], v[106:107], v[64:65], v[126:127] op_sel_hi:[0,1,1]
	v_cndmask_b32_e64 v100, 0, v18, s[10:11]
	v_cndmask_b32_e64 v101, 0, v18, s[14:15]
	v_add_f32_dpp v126, v50, v126 wave_shl:1 row_mask:0xf bank_mask:0xf bound_ctrl:1
	v_add_f32_dpp v127, v51, v127 wave_shl:1 row_mask:0xf bank_mask:0xf bound_ctrl:1
	s_add_i32 s4, s34, 2
	s_cmpk_lt_i32 s4, 0x201
	s_cselect_b64 s[12:13], s[0:1], 0
	v_add_f32_dpp v126, v66, v126 wave_shr:1 row_mask:0xf bank_mask:0xf bound_ctrl:1
	v_add_f32_dpp v127, v67, v127 wave_shr:1 row_mask:0xf bank_mask:0xf bound_ctrl:1
	v_pk_fma_f32 v[126:127], v[92:93], v[146:147], v[126:127] op_sel_hi:[1,0,1] neg_lo:[0,0,1] neg_hi:[0,0,1]
	v_pk_add_f32 v[126:127], v[126:127], v[100:101] neg_lo:[0,1] neg_hi:[0,1]
	v_pk_mul_f32 v[116:117], v[126:127], v[126:127]
	v_add_f32_e32 v116, v116, v117
	v_cndmask_b32_e64 v117, 0, v116, s[12:13]
	v_add_f32_e32 v1, v1, v117
	s_waitcnt vmcnt(8)
	v_mov_b32_dpp v12, v172 wave_shr:1 row_mask:0xf bank_mask:0xf bound_ctrl:1
	v_mov_b32_dpp v13, v173 wave_shr:1 row_mask:0xf bank_mask:0xf bound_ctrl:1
	v_mov_b32_dpp v14, v174 wave_shr:1 row_mask:0xf bank_mask:0xf bound_ctrl:1
	v_mov_b32_dpp v64, v172 wave_shl:1 row_mask:0xf bank_mask:0xf bound_ctrl:1
	v_mov_b32_dpp v65, v173 wave_shl:1 row_mask:0xf bank_mask:0xf bound_ctrl:1
	v_mov_b32_dpp v66, v174 wave_shl:1 row_mask:0xf bank_mask:0xf bound_ctrl:1
	v_pk_add_f32 v[4:5], v[172:173], v[12:13]
	v_pk_mul_f32 v[44:45], v[172:173], v[172:173] op_sel_hi:[0,1]
	v_pk_mul_f32 v[50:51], v[172:173], v[174:175] op_sel_hi:[1,0]
	v_mul_f32_e64 v80, v173, v173
	v_mul_f32_e64 v81, v174, v174
	v_add_f32_e64 v82, v174, v14
	v_pk_add_f32 v[4:5], v[4:5], v[64:65]
	v_or3_b32 v29, v58, v59, v56
	v_or3_b32 v29, v29, v49, v57
	s_add_i32 s4, s34, 3
	s_cmpk_lt_u32 s4, 0x1ff
	s_cselect_b64 s[12:13], s[42:43], 0
	v_cmp_ne_u32_e64 s[30:31], 0, v29
	s_and_b64 s[30:31], s[30:31], s[12:13]
	v_cndmask_b32_e64 v29, 0, 1.0, s[30:31]
	v_pk_fma_f32 v[44:45], v[12:13], v[12:13], v[44:45] op_sel_hi:[0,1,1]
	v_pk_fma_f32 v[50:51], v[12:13], v[14:15], v[50:51] op_sel_hi:[1,0,1]
	v_fma_f32 v80, v13, v13, v80
	v_fma_f32 v81, v14, v14, v81
	v_add_f32_dpp v83, v29, v29 wave_shr:1 row_mask:0xf bank_mask:0xf bound_ctrl:1
	v_add_f32_e64 v82, v82, v66
	v_pk_fma_f32 v[44:45], v[64:65], v[64:65], v[44:45] op_sel_hi:[0,1,1]
	v_pk_fma_f32 v[50:51], v[64:65], v[66:67], v[50:51] op_sel_hi:[1,0,1]
	v_fma_f32 v80, v65, v65, v80
	v_fma_f32 v81, v66, v66, v81
	v_add_f32_dpp v83, v29, v83 wave_shl:1 row_mask:0xf bank_mask:0xf bound_ctrl:1
	v_pk_add_f32 v[92:93], v[84:85], v[4:5]
	v_pk_add_f32 v[84:85], v[6:7], v[44:45]
	v_pk_add_f32 v[6:7], v[52:53], v[50:51]
	v_pk_add_f32 v[52:53], v[112:113], v[80:81]
	v_pk_add_f32 v[100:101], v[124:125], v[82:83]
	v_mul_f32_e64 v104, v92, v22
	v_mul_f32_e64 v105, v93, v22
	v_mul_f32_e64 v106, v100, v22
	v_fma_f32 v29, v84, v22, v26
	v_mul_f32_e64 v48, v85, v22
	v_mul_f32_e64 v112, v6, v22
	v_fma_f32 v113, v52, v22, v26
	v_mul_f32_e64 v116, v7, v22
	v_fma_f32 v117, v53, v22, v26
	v_fma_f32 v29, -v104, v104, v29
	v_fma_f32 v48, -v104, v105, v48
	v_fma_f32 v112, -v104, v106, v112
	v_fma_f32 v113, -v105, v105, v113
	v_fma_f32 v116, -v105, v106, v116
	v_fma_f32 v117, -v106, v106, v117
	v_mul_f32_e64 v120, v116, v116
	v_mul_f32_e64 v121, v48, v117
	v_mul_f32_e64 v132, v112, v113
	v_mul_f32_e64 v133, v112, v112
	v_mul_f32_e64 v134, v29, v116
	v_mul_f32_e64 v135, v48, v48
	v_fma_f32 v120, v113, v117, -v120
	v_fma_f32 v121, v112, v116, -v121
	v_fma_f32 v132, v48, v116, -v132
	v_fma_f32 v133, v29, v117, -v133
	v_fma_f32 v134, v48, v112, -v134
	v_fma_f32 v135, v29, v113, -v135
	v_mul_f32_e64 v140, v29, v120
	v_fma_f32 v140, v48, v121, v140
	v_fma_f32 v140, v112, v132, v140
	v_rcp_f32_e32 v140, v140
	v_cmp_ne_u32_e64 vcc, s37, v24
	v_mul_f32_e64 v140, v140, v22
	v_cndmask_b32_e64 v140, 0, v140, s[30:31]
	v_cndmask_b32_e64 v29, 0, v18, vcc
	v_cndmask_b32_e64 v129, 0, v22, s[30:31]
	v_mul_f32_e64 v107, v120, v140
	v_mul_f32_e64 v124, v121, v140
	v_mul_f32_e64 v125, v132, v140
	v_mul_f32_e64 v126, v133, v140
	v_mul_f32_e64 v127, v134, v140
	v_mul_f32_e64 v128, v135, v140
	v_add_f32_e64 v130, v101, v29
	v_mov_b32_e32 v131, v24
	ds_write_b128 v23, v[104:107] offset:3072
	ds_write_b128 v23, v[124:127] offset:4096
	ds_write_b128 v23, v[128:131] offset:5120
	v_mov_b32_dpp v52, v46 wave_shr:1 row_mask:0xf bank_mask:0xf bound_ctrl:1
	v_mov_b32_dpp v53, v47 wave_shr:1 row_mask:0xf bank_mask:0xf bound_ctrl:1
	v_mov_b32_dpp v84, v46 wave_shl:1 row_mask:0xf bank_mask:0xf bound_ctrl:1
	v_mov_b32_dpp v85, v47 wave_shl:1 row_mask:0xf bank_mask:0xf bound_ctrl:1
	v_pk_mul_f32 v[6:7], v[46:47], v[172:173] op_sel_hi:[1,0]
	v_pk_mul_f32 v[134:135], v[46:47], v[172:173] op_sel:[0,1]
	v_pk_mul_f32 v[142:143], v[46:47], v[174:175] op_sel_hi:[1,0]
	v_pk_add_f32 v[146:147], v[46:47], v[52:53]
	v_pk_fma_f32 v[6:7], v[52:53], v[12:13], v[6:7] op_sel_hi:[1,0,1]
	v_pk_fma_f32 v[134:135], v[52:53], v[12:13], v[134:135] op_sel:[0,1,0]
	v_pk_fma_f32 v[142:143], v[52:53], v[14:15], v[142:143] op_sel_hi:[1,0,1]
	v_pk_add_f32 v[146:147], v[146:147], v[84:85]
	v_pk_fma_f32 v[6:7], v[84:85], v[64:65], v[6:7] op_sel_hi:[1,0,1]
	v_pk_fma_f32 v[134:135], v[84:85], v[64:65], v[134:135] op_sel:[0,1,0]
	v_pk_fma_f32 v[142:143], v[84:85], v[66:67], v[142:143] op_sel_hi:[1,0,1]
	s_waitcnt lgkmcnt(0)
	s_barrier
	s_add_i32 s5, s34, 8
	s_min_i32 s5, s5, 0x200
	s_mul_i32 s6, s5, 0x804
	s_add_i32 s6, s6, s35
	s_add_i32 s7, s6, 0x505014
	s_add_i32 s8, s6, 0x606018
	s_mul_i32 s9, s5, 0x180c
	s_add_i32 s9, s9, s33
	s_add_i32 s4, s34, 9
	s_min_i32 s4, s4, 0x200
	s_mul_i32 s4, s4, 0x804
	s_add_i32 s4, s4, s38
	buffer_load_dword v24, v28, s[20:23], s4 offen nt
	buffer_load_dwordx3 v[156:158], v27, s[24:27], s9 offen nt
	buffer_load_dword v52, v28, s[16:19], s7 offen nt
	buffer_load_dword v53, v28, s[16:19], s8 offen nt
	s_waitcnt vmcnt(8)
	s_add_i32 s4, s34, 7
	s_cmpk_lt_u32 s4, 0x201
	s_cselect_b64 s[12:13], s[40:41], 0
	v_cmp_eq_u32_e64 s[14:15], s37, v17
	s_and_b64 s[14:15], s[14:15], s[12:13]
	v_cndmask_b32_e64 v29, 0, 1, s[14:15]
	s_nop 1
	v_or_b32_dpp v48, v29, v29 wave_shr:1 row_mask:0xf bank_mask:0xf bound_ctrl:1
	s_nop 1
	v_or_b32_dpp v48, v29, v48 wave_shl:1 row_mask:0xf bank_mask:0xf bound_ctrl:1
	s_nop 1
	v_or_b32_dpp v57, v48, v48 wave_shr:1 row_mask:0xf bank_mask:0xf bound_ctrl:1
	s_nop 1
	v_or_b32_dpp v57, v48, v57 wave_shl:1 row_mask:0xf bank_mask:0xf bound_ctrl:1
	v_pk_add_f32 v[84:85], v[70:71], v[146:147]
	v_pk_add_f32 v[70:71], v[90:91], v[6:7]
	v_pk_add_f32 v[90:91], v[86:87], v[134:135]
	v_pk_add_f32 v[86:87], v[94:95], v[142:143]
	v_pk_fma_f32 v[70:71], v[104:105], v[84:85], v[70:71] op_sel_hi:[0,1,1] neg_lo:[1,0,0] neg_hi:[1,0,0]
	v_pk_fma_f32 v[90:91], v[104:105], v[84:85], v[90:91] op_sel:[1,0,0] neg_lo:[1,0,0] neg_hi:[1,0,0]
	v_pk_fma_f32 v[86:87], v[106:107], v[84:85], v[86:87] op_sel_hi:[0,1,1] neg_lo:[1,0,0] neg_hi:[1,0,0]
	v_pk_mul_f32 v[92:93], v[106:107], v[70:71] op_sel:[1,0]
	v_pk_mul_f32 v[100:101], v[124:125], v[70:71] op_sel_hi:[0,1]
	v_pk_mul_f32 v[112:113], v[124:125], v[70:71] op_sel:[1,0]
	v_pk_fma_f32 v[92:93], v[124:125], v[90:91], v[92:93] op_sel_hi:[0,1,1]
	v_pk_fma_f32 v[100:101], v[126:127], v[90:91], v[100:101] op_sel_hi:[0,1,1]
	v_pk_fma_f32 v[112:113], v[126:127], v[90:91], v[112:113] op_sel:[1,0,0]
	v_pk_fma_f32 v[92:93], v[124:125], v[86:87], v[92:93] op_sel:[1,0,0]
	v_pk_fma_f32 v[100:101], v[126:127], v[86:87], v[100:101] op_sel:[1,0,0]
	v_pk_fma_f32 v[112:113], v[128:129], v[86:87], v[112:113] op_sel_hi:[0,1,1]
	v_pk_mul_f32 v[94:95], v[104:105], v[92:93] op_sel_hi:[0,1]
	v_pk_fma_f32 v[94:95], v[104:105], v[100:101], v[94:95] op_sel:[1,0,0]
	v_pk_fma_f32 v[94:95], v[106:107], v[112:113], v[94:95] op_sel_hi:[0,1,1]
	v_pk_fma_f32 v[94:95], v[128:129], v[84:85], v[94:95] op_sel:[1,0,0] neg_lo:[0,0,1] neg_hi:[0,0,1]
	v_cmp_eq_u32_e64 s[10:11], 6, v131
	v_cmp_eq_u32_e64 s[14:15], 7, v131
	v_pk_add_f32 v[70:71], v[74:75], v[92:93]
	v_pk_add_f32 v[74:75], v[118:119], v[100:101]
	v_pk_add_f32 v[84:85], v[122:123], v[112:113]
	v_pk_add_f32 v[116:117], v[88:89], v[94:95]
	v_pk_fma_f32 v[88:89], v[32:33], v[70:71], v[116:117] op_sel_hi:[0,1,1]
	v_pk_fma_f32 v[120:121], v[108:109], v[70:71], v[116:117] op_sel_hi:[0,1,1]
	v_pk_fma_f32 v[88:89], v[32:33], v[74:75], v[88:89] op_sel:[1,0,0]
	v_pk_fma_f32 v[120:121], v[108:109], v[74:75], v[120:121] op_sel:[1,0,0]
	v_pk_fma_f32 v[88:89], v[34:35], v[84:85], v[88:89] op_sel_hi:[0,1,1]
	v_pk_fma_f32 v[120:121], v[110:111], v[84:85], v[120:121] op_sel_hi:[0,1,1]
	v_pk_fma_f32 v[116:117], v[152:153], v[70:71], v[116:117] op_sel_hi:[0,1,1]
	v_pk_fma_f32 v[116:117], v[152:153], v[74:75], v[116:117] op_sel:[1,0,0]
	v_pk_fma_f32 v[116:117], v[154:155], v[84:85], v[116:117] op_sel_hi:[0,1,1]
	v_cndmask_b32_e64 v86, 0, v18, s[10:11]
	v_cndmask_b32_e64 v87, 0, v18, s[14:15]
	v_add_f32_dpp v116, v88, v116 wave_shl:1 row_mask:0xf bank_mask:0xf bound_ctrl:1
	v_add_f32_dpp v117, v89, v117 wave_shl:1 row_mask:0xf bank_mask:0xf bound_ctrl:1
	s_add_i32 s4, s34, 3
	s_cmpk_lt_i32 s4, 0x201
	s_cselect_b64 s[12:13], s[0:1], 0
	v_add_f32_dpp v116, v120, v116 wave_shr:1 row_mask:0xf bank_mask:0xf bound_ctrl:1
	v_add_f32_dpp v117, v121, v117 wave_shr:1 row_mask:0xf bank_mask:0xf bound_ctrl:1
	v_pk_fma_f32 v[116:117], v[54:55], v[130:131], v[116:117] op_sel_hi:[1,0,1] neg_lo:[0,0,1] neg_hi:[0,0,1]
	v_pk_add_f32 v[116:117], v[116:117], v[86:87] neg_lo:[0,1] neg_hi:[0,1]
	v_pk_mul_f32 v[90:91], v[116:117], v[116:117]
	v_add_f32_e32 v90, v90, v91
	v_cndmask_b32_e64 v91, 0, v90, s[12:13]
	v_add_f32_e32 v1, v1, v91
	s_waitcnt vmcnt(8)
	v_mov_b32_dpp v32, v148 wave_shr:1 row_mask:0xf bank_mask:0xf bound_ctrl:1
	v_mov_b32_dpp v33, v149 wave_shr:1 row_mask:0xf bank_mask:0xf bound_ctrl:1
	v_mov_b32_dpp v34, v150 wave_shr:1 row_mask:0xf bank_mask:0xf bound_ctrl:1
	v_mov_b32_dpp v84, v148 wave_shl:1 row_mask:0xf bank_mask:0xf bound_ctrl:1
	v_mov_b32_dpp v85, v149 wave_shl:1 row_mask:0xf bank_mask:0xf bound_ctrl:1
	v_mov_b32_dpp v86, v150 wave_shl:1 row_mask:0xf bank_mask:0xf bound_ctrl:1
	v_pk_add_f32 v[54:55], v[148:149], v[32:33]
	v_pk_mul_f32 v[70:71], v[148:149], v[148:149] op_sel_hi:[0,1]
	v_pk_mul_f32 v[74:75], v[148:149], v[150:151] op_sel_hi:[1,0]
	v_mul_f32_e64 v88, v149, v149
	v_mul_f32_e64 v89, v150, v150
	v_add_f32_e64 v90, v150, v34
	v_pk_add_f32 v[54:55], v[54:55], v[84:85]
	v_or3_b32 v29, v57, v58, v59
	v_or3_b32 v29, v29, v56, v49
	s_add_i32 s4, s34, 4
	s_cmpk_lt_u32 s4, 0x1ff
	s_cselect_b64 s[12:13], s[42:43], 0
	v_cmp_ne_u32_e64 s[30:31], 0, v29
	s_and_b64 s[30:31], s[30:31], s[12:13]
	v_cndmask_b32_e64 v29, 0, 1.0, s[30:31]
	v_pk_fma_f32 v[70:71], v[32:33], v[32:33], v[70:71] op_sel_hi:[0,1,1]
	v_pk_fma_f32 v[74:75], v[32:33], v[34:35], v[74:75] op_sel_hi:[1,0,1]
	v_fma_f32 v88, v33, v33, v88
	v_fma_f32 v89, v34, v34, v89
	v_add_f32_dpp v91, v29, v29 wave_shr:1 row_mask:0xf bank_mask:0xf bound_ctrl:1
	v_add_f32_e64 v90, v90, v86
	v_pk_fma_f32 v[70:71], v[84:85], v[84:85], v[70:71] op_sel_hi:[0,1,1]
	v_pk_fma_f32 v[74:75], v[84:85], v[86:87], v[74:75] op_sel_hi:[1,0,1]
	v_fma_f32 v88, v85, v85, v88
	v_fma_f32 v89, v86, v86, v89
	v_add_f32_dpp v91, v29, v91 wave_shl:1 row_mask:0xf bank_mask:0xf bound_ctrl:1
	v_pk_add_f32 v[104:105], v[4:5], v[54:55]
	v_pk_add_f32 v[106:107], v[30:31], v[104:105]
	v_pk_add_f32 v[4:5], v[44:45], v[70:71]
	v_pk_add_f32 v[30:31], v[38:39], v[4:5]
	v_pk_add_f32 v[38:39], v[50:51], v[74:75]
	v_pk_add_f32 v[44:45], v[72:73], v[38:39]
	v_pk_add_f32 v[50:51], v[80:81], v[88:89]
	v_pk_add_f32 v[72:73], v[76:77], v[50:51]
	v_pk_add_f32 v[76:77], v[82:83], v[90:91]
	v_pk_add_f32 v[80:81], v[78:79], v[76:77]
	v_mul_f32_e64 v108, v106, v22
	v_mul_f32_e64 v109, v107, v22
	v_mul_f32_e64 v110, v80, v22
	v_fma_f32 v29, v30, v22, v26
	v_mul_f32_e64 v48, v31, v22
	v_mul_f32_e64 v78, v44, v22
	v_fma_f32 v79, v72, v22, v26
	v_mul_f32_e64 v82, v45, v22
	v_fma_f32 v83, v73, v22, v26
	v_fma_f32 v29, -v108, v108, v29
	v_fma_f32 v48, -v108, v109, v48
	v_fma_f32 v78, -v108, v110, v78
	v_fma_f32 v79, -v109, v109, v79
	v_fma_f32 v82, -v109, v110, v82
	v_fma_f32 v83, -v110, v110, v83
	v_mul_f32_e64 v124, v82, v82
	v_mul_f32_e64 v125, v48, v83
	v_mul_f32_e64 v126, v78, v79
	v_mul_f32_e64 v127, v78, v78
	v_mul_f32_e64 v128, v29, v82
	v_mul_f32_e64 v129, v48, v48
	v_fma_f32 v124, v79, v83, -v124
	v_fma_f32 v125, v78, v82, -v125
	v_fma_f32 v126, v48, v82, -v126
	v_fma_f32 v127, v29, v83, -v127
	v_fma_f32 v128, v48, v78, -v128
	v_fma_f32 v129, v29, v79, -v129
	v_mul_f32_e64 v130, v29, v124
	v_fma_f32 v130, v48, v125, v130
	v_fma_f32 v130, v78, v126, v130
	v_rcp_f32_e32 v130, v130
	v_cmp_ne_u32_e64 vcc, s37, v2
	v_mul_f32_e64 v130, v130, v22
	v_cndmask_b32_e64 v130, 0, v130, s[30:31]
	v_cndmask_b32_e64 v29, 0, v18, vcc
	v_cndmask_b32_e64 v121, 0, v22, s[30:31]
	v_mul_f32_e64 v111, v124, v130
	v_mul_f32_e64 v116, v125, v130
	v_mul_f32_e64 v117, v126, v130
	v_mul_f32_e64 v118, v127, v130
	v_mul_f32_e64 v119, v128, v130
	v_mul_f32_e64 v120, v129, v130
	v_add_f32_e64 v122, v81, v29
	v_mov_b32_e32 v123, v2
	ds_write_b128 v23, v[108:111]
	ds_write_b128 v23, v[116:119] offset:1024
	ds_write_b128 v23, v[120:123] offset:2048
	v_mov_b32_dpp v30, v96 wave_shr:1 row_mask:0xf bank_mask:0xf bound_ctrl:1
	v_mov_b32_dpp v31, v97 wave_shr:1 row_mask:0xf bank_mask:0xf bound_ctrl:1
	v_mov_b32_dpp v78, v96 wave_shl:1 row_mask:0xf bank_mask:0xf bound_ctrl:1
	v_mov_b32_dpp v79, v97 wave_shl:1 row_mask:0xf bank_mask:0xf bound_ctrl:1
	v_pk_mul_f32 v[44:45], v[96:97], v[148:149] op_sel_hi:[1,0]
	v_pk_mul_f32 v[48:49], v[96:97], v[148:149] op_sel:[0,1]
	v_pk_mul_f32 v[72:73], v[96:97], v[150:151] op_sel_hi:[1,0]
	v_pk_add_f32 v[80:81], v[96:97], v[30:31]
	v_pk_fma_f32 v[44:45], v[30:31], v[32:33], v[44:45] op_sel_hi:[1,0,1]
	v_pk_fma_f32 v[48:49], v[30:31], v[32:33], v[48:49] op_sel:[0,1,0]
	v_pk_fma_f32 v[72:73], v[30:31], v[34:35], v[72:73] op_sel_hi:[1,0,1]
	v_pk_add_f32 v[80:81], v[80:81], v[78:79]
	v_pk_fma_f32 v[44:45], v[78:79], v[84:85], v[44:45] op_sel_hi:[1,0,1]
	v_pk_fma_f32 v[48:49], v[78:79], v[84:85], v[48:49] op_sel:[0,1,0]
	v_pk_fma_f32 v[72:73], v[78:79], v[86:87], v[72:73] op_sel_hi:[1,0,1]
	s_waitcnt lgkmcnt(0)
	s_barrier
	s_add_i32 s5, s34, 9
	s_min_i32 s5, s5, 0x200
	s_mul_i32 s6, s5, 0x804
	s_add_i32 s6, s6, s35
	s_add_i32 s7, s6, 0x505014
	s_add_i32 s8, s6, 0x606018
	s_mul_i32 s9, s5, 0x180c
	s_add_i32 s9, s9, s33
	s_add_i32 s4, s34, 10
	s_min_i32 s4, s4, 0x200
	s_mul_i32 s4, s4, 0x804
	s_add_i32 s4, s4, s38
	buffer_load_dword v2, v28, s[20:23], s4 offen nt
	buffer_load_dwordx3 v[124:126], v27, s[24:27], s9 offen nt
	buffer_load_dword v30, v28, s[16:19], s7 offen nt
	buffer_load_dword v31, v28, s[16:19], s8 offen nt
	s_waitcnt vmcnt(8)
	s_add_i32 s4, s34, 8
	s_cmpk_lt_u32 s4, 0x201
	s_cselect_b64 s[12:13], s[40:41], 0
	v_cmp_eq_u32_e64 s[14:15], s37, v25
	s_and_b64 s[14:15], s[14:15], s[12:13]
	v_cndmask_b32_e64 v29, 0, 1, s[14:15]
	s_nop 1
	v_or_b32_dpp v78, v29, v29 wave_shr:1 row_mask:0xf bank_mask:0xf bound_ctrl:1
	s_nop 1
	v_or_b32_dpp v78, v29, v78 wave_shl:1 row_mask:0xf bank_mask:0xf bound_ctrl:1
	s_nop 1
	v_or_b32_dpp v79, v78, v78 wave_shr:1 row_mask:0xf bank_mask:0xf bound_ctrl:1
	s_nop 1
	v_or_b32_dpp v79, v78, v79 wave_shl:1 row_mask:0xf bank_mask:0xf bound_ctrl:1
	v_pk_add_f32 v[82:83], v[146:147], v[80:81]
	v_pk_add_f32 v[106:107], v[164:165], v[82:83]
	v_pk_add_f32 v[130:131], v[6:7], v[44:45]
	v_pk_add_f32 v[128:129], v[20:21], v[130:131]
	v_pk_add_f32 v[6:7], v[134:135], v[48:49]
	v_pk_add_f32 v[20:21], v[68:69], v[6:7]
	v_pk_add_f32 v[134:135], v[142:143], v[72:73]
	v_pk_add_f32 v[68:69], v[160:161], v[134:135]
	v_pk_fma_f32 v[128:129], v[108:109], v[106:107], v[128:129] op_sel_hi:[0,1,1] neg_lo:[1,0,0] neg_hi:[1,0,0]
	v_pk_fma_f32 v[20:21], v[108:109], v[106:107], v[20:21] op_sel:[1,0,0] neg_lo:[1,0,0] neg_hi:[1,0,0]
	v_pk_fma_f32 v[68:69], v[110:111], v[106:107], v[68:69] op_sel_hi:[0,1,1] neg_lo:[1,0,0] neg_hi:[1,0,0]
	v_pk_mul_f32 v[142:143], v[110:111], v[128:129] op_sel:[1,0]
	v_pk_mul_f32 v[146:147], v[116:117], v[128:129] op_sel_hi:[0,1]
	v_pk_mul_f32 v[154:155], v[116:117], v[128:129] op_sel:[1,0]
	v_pk_fma_f32 v[142:143], v[116:117], v[20:21], v[142:143] op_sel_hi:[0,1,1]
	v_pk_fma_f32 v[146:147], v[118:119], v[20:21], v[146:147] op_sel_hi:[0,1,1]
	v_pk_fma_f32 v[154:155], v[118:119], v[20:21], v[154:155] op_sel:[1,0,0]
	v_pk_fma_f32 v[142:143], v[116:117], v[68:69], v[142:143] op_sel:[1,0,0]
	v_pk_fma_f32 v[146:147], v[118:119], v[68:69], v[146:147] op_sel:[1,0,0]
	v_pk_fma_f32 v[154:155], v[120:121], v[68:69], v[154:155] op_sel_hi:[0,1,1]
	v_pk_mul_f32 v[132:133], v[108:109], v[142:143] op_sel_hi:[0,1]
	v_pk_fma_f32 v[132:133], v[108:109], v[146:147], v[132:133] op_sel:[1,0,0]
	v_pk_fma_f32 v[132:133], v[110:111], v[154:155], v[132:133] op_sel_hi:[0,1,1]
	v_pk_fma_f32 v[132:133], v[120:121], v[106:107], v[132:133] op_sel:[1,0,0] neg_lo:[0,0,1] neg_hi:[0,0,1]
	v_cmp_eq_u32_e64 s[10:11], 6, v123
	v_cmp_eq_u32_e64 s[14:15], 7, v123
	v_pk_add_f32 v[20:21], v[92:93], v[142:143]
	v_pk_add_f32 v[68:69], v[98:99], v[20:21]
	v_pk_add_f32 v[92:93], v[100:101], v[146:147]
	v_pk_add_f32 v[98:99], v[102:103], v[92:93]
	v_pk_add_f32 v[100:101], v[112:113], v[154:155]
	v_pk_add_f32 v[102:103], v[114:115], v[100:101]
	v_pk_add_f32 v[106:107], v[94:95], v[132:133]
	v_pk_add_f32 v[112:113], v[60:61], v[106:107]
	v_pk_fma_f32 v[60:61], v[8:9], v[68:69], v[112:113] op_sel_hi:[0,1,1]
	v_pk_fma_f32 v[128:129], v[40:41], v[68:69], v[112:113] op_sel_hi:[0,1,1]
	v_pk_fma_f32 v[60:61], v[8:9], v[98:99], v[60:61] op_sel:[1,0,0]
	v_pk_fma_f32 v[128:129], v[40:41], v[98:99], v[128:129] op_sel:[1,0,0]
	v_pk_fma_f32 v[60:61], v[10:11], v[102:103], v[60:61] op_sel_hi:[0,1,1]
	v_pk_fma_f32 v[128:129], v[42:43], v[102:103], v[128:129] op_sel_hi:[0,1,1]
	v_pk_fma_f32 v[112:113], v[136:137], v[68:69], v[112:113] op_sel_hi:[0,1,1]
	v_pk_fma_f32 v[112:113], v[136:137], v[98:99], v[112:113] op_sel:[1,0,0]
	v_pk_fma_f32 v[112:113], v[138:139], v[102:103], v[112:113] op_sel_hi:[0,1,1]
	v_cndmask_b32_e64 v94, 0, v18, s[10:11]
	v_cndmask_b32_e64 v95, 0, v18, s[14:15]
	v_add_f32_dpp v112, v60, v112 wave_shl:1 row_mask:0xf bank_mask:0xf bound_ctrl:1
	v_add_f32_dpp v113, v61, v113 wave_shl:1 row_mask:0xf bank_mask:0xf bound_ctrl:1
	s_add_i32 s4, s34, 4
	s_cmpk_lt_i32 s4, 0x201
	s_cselect_b64 s[12:13], s[0:1], 0
	v_add_f32_dpp v112, v128, v112 wave_shr:1 row_mask:0xf bank_mask:0xf bound_ctrl:1
	v_add_f32_dpp v113, v129, v113 wave_shr:1 row_mask:0xf bank_mask:0xf bound_ctrl:1
	v_pk_fma_f32 v[112:113], v[36:37], v[122:123], v[112:113] op_sel_hi:[1,0,1] neg_lo:[0,0,1] neg_hi:[0,0,1]
	v_pk_add_f32 v[112:113], v[112:113], v[94:95] neg_lo:[0,1] neg_hi:[0,1]
	v_pk_mul_f32 v[114:115], v[112:113], v[112:113]
	v_add_f32_e32 v114, v114, v115
	v_cndmask_b32_e64 v115, 0, v114, s[12:13]
	v_add_f32_e32 v1, v1, v115
	s_waitcnt vmcnt(8)
	v_mov_b32_dpp v8, v168 wave_shr:1 row_mask:0xf bank_mask:0xf bound_ctrl:1
	v_mov_b32_dpp v9, v169 wave_shr:1 row_mask:0xf bank_mask:0xf bound_ctrl:1
	v_mov_b32_dpp v10, v170 wave_shr:1 row_mask:0xf bank_mask:0xf bound_ctrl:1
	v_mov_b32_dpp v40, v168 wave_shl:1 row_mask:0xf bank_mask:0xf bound_ctrl:1
	v_mov_b32_dpp v41, v169 wave_shl:1 row_mask:0xf bank_mask:0xf bound_ctrl:1
	v_mov_b32_dpp v42, v170 wave_shl:1 row_mask:0xf bank_mask:0xf bound_ctrl:1
	v_pk_add_f32 v[36:37], v[168:169], v[8:9]
	v_pk_mul_f32 v[60:61], v[168:169], v[168:169] op_sel_hi:[0,1]
	v_pk_mul_f32 v[68:69], v[168:169], v[170:171] op_sel_hi:[1,0]
	v_mul_f32_e64 v94, v169, v169
	v_mul_f32_e64 v95, v170, v170
	v_add_f32_e64 v98, v170, v10
	v_pk_add_f32 v[36:37], v[36:37], v[40:41]
	v_or3_b32 v29, v79, v57, v58
	v_or3_b32 v29, v29, v59, v56
	s_add_i32 s4, s34, 5
	s_cmpk_lt_u32 s4, 0x1ff
	s_cselect_b64 s[12:13], s[42:43], 0
	v_cmp_ne_u32_e64 s[30:31], 0, v29
	s_and_b64 s[30:31], s[30:31], s[12:13]
	v_cndmask_b32_e64 v29, 0, 1.0, s[30:31]
	v_pk_fma_f32 v[60:61], v[8:9], v[8:9], v[60:61] op_sel_hi:[0,1,1]
	v_pk_fma_f32 v[68:69], v[8:9], v[10:11], v[68:69] op_sel_hi:[1,0,1]
	v_fma_f32 v94, v9, v9, v94
	v_fma_f32 v95, v10, v10, v95
	v_add_f32_dpp v99, v29, v29 wave_shr:1 row_mask:0xf bank_mask:0xf bound_ctrl:1
	v_add_f32_e64 v98, v98, v42
	v_pk_fma_f32 v[60:61], v[40:41], v[40:41], v[60:61] op_sel_hi:[0,1,1]
	v_pk_fma_f32 v[68:69], v[40:41], v[42:43], v[68:69] op_sel_hi:[1,0,1]
	v_fma_f32 v94, v41, v41, v94
	v_fma_f32 v95, v42, v42, v95
	v_add_f32_dpp v99, v29, v99 wave_shl:1 row_mask:0xf bank_mask:0xf bound_ctrl:1
	v_pk_add_f32 v[102:103], v[104:105], v[36:37]
	v_pk_add_f32 v[104:105], v[4:5], v[60:61]
	v_pk_add_f32 v[4:5], v[38:39], v[68:69]
	v_pk_add_f32 v[38:39], v[50:51], v[94:95]
	v_pk_add_f32 v[50:51], v[76:77], v[98:99]
	v_mul_f32_e64 v108, v102, v22
	v_mul_f32_e64 v109, v103, v22
	v_mul_f32_e64 v110, v50, v22
	v_fma_f32 v29, v104, v22, v26
	v_mul_f32_e64 v78, v105, v22
	v_mul_f32_e64 v76, v4, v22
	v_fma_f32 v77, v38, v22, v26
	v_mul_f32_e64 v120, v5, v22
	v_fma_f32 v121, v39, v22, v26
	v_fma_f32 v29, -v108, v108, v29
	v_fma_f32 v78, -v108, v109, v78
	v_fma_f32 v76, -v108, v110, v76
	v_fma_f32 v77, -v109, v109, v77
	v_fma_f32 v120, -v109, v110, v120
	v_fma_f32 v121, -v110, v110, v121
	v_mul_f32_e64 v122, v120, v120
	v_mul_f32_e64 v123, v78, v121
	v_mul_f32_e64 v128, v76, v77
	v_mul_f32_e64 v129, v76, v76
	v_mul_f32_e64 v136, v29, v120
	v_mul_f32_e64 v137, v78, v78
	v_fma_f32 v122, v77, v121, -v122
	v_fma_f32 v123, v76, v120, -v123
	v_fma_f32 v128, v78, v120, -v128
	v_fma_f32 v129, v29, v121, -v129
	v_fma_f32 v136, v78, v76, -v136
	v_fma_f32 v137, v29, v77, -v137
	v_mul_f32_e64 v138, v29, v122
	v_fma_f32 v138, v78, v123, v138
	v_fma_f32 v138, v76, v128, v138
	v_rcp_f32_e32 v138, v138
	v_cmp_ne_u32_e64 vcc, s37, v3
	v_mul_f32_e64 v138, v138, v22
	v_cndmask_b32_e64 v138, 0, v138, s[30:31]
	v_cndmask_b32_e64 v29, 0, v18, vcc
	v_cndmask_b32_e64 v117, 0, v22, s[30:31]
	v_mul_f32_e64 v111, v122, v138
	v_mul_f32_e64 v112, v123, v138
	v_mul_f32_e64 v113, v128, v138
	v_mul_f32_e64 v114, v129, v138
	v_mul_f32_e64 v115, v136, v138
	v_mul_f32_e64 v116, v137, v138
	v_add_f32_e64 v118, v51, v29
	v_mov_b32_e32 v119, v3
	ds_write_b128 v23, v[108:111] offset:3072
	ds_write_b128 v23, v[112:115] offset:4096
	ds_write_b128 v23, v[116:119] offset:5120
	v_mov_b32_dpp v4, v62 wave_shr:1 row_mask:0xf bank_mask:0xf bound_ctrl:1
	v_mov_b32_dpp v5, v63 wave_shr:1 row_mask:0xf bank_mask:0xf bound_ctrl:1
	v_mov_b32_dpp v76, v62 wave_shl:1 row_mask:0xf bank_mask:0xf bound_ctrl:1
	v_mov_b32_dpp v77, v63 wave_shl:1 row_mask:0xf bank_mask:0xf bound_ctrl:1
	v_pk_mul_f32 v[38:39], v[62:63], v[168:169] op_sel_hi:[1,0]
	v_pk_mul_f32 v[50:51], v[62:63], v[168:169] op_sel:[0,1]
	v_pk_mul_f32 v[102:103], v[62:63], v[170:171] op_sel_hi:[1,0]
	v_pk_add_f32 v[122:123], v[62:63], v[4:5]
	v_pk_fma_f32 v[38:39], v[4:5], v[8:9], v[38:39] op_sel_hi:[1,0,1]
	v_pk_fma_f32 v[50:51], v[4:5], v[8:9], v[50:51] op_sel:[0,1,0]
	v_pk_fma_f32 v[102:103], v[4:5], v[10:11], v[102:103] op_sel_hi:[1,0,1]
	v_pk_add_f32 v[122:123], v[122:123], v[76:77]
	v_pk_fma_f32 v[38:39], v[76:77], v[40:41], v[38:39] op_sel_hi:[1,0,1]
	v_pk_fma_f32 v[50:51], v[76:77], v[40:41], v[50:51] op_sel:[0,1,0]
	v_pk_fma_f32 v[102:103], v[76:77], v[42:43], v[102:103] op_sel_hi:[1,0,1]
	s_waitcnt lgkmcnt(0)
	s_barrier
	s_add_i32 s5, s34, 10
	s_min_i32 s5, s5, 0x200
	s_mul_i32 s6, s5, 0x804
	s_add_i32 s6, s6, s35
	s_add_i32 s7, s6, 0x505014
	s_add_i32 s8, s6, 0x606018
	s_mul_i32 s9, s5, 0x180c
	s_add_i32 s9, s9, s33
	s_add_i32 s4, s34, 11
	s_min_i32 s4, s4, 0x200
	s_mul_i32 s4, s4, 0x804
	s_add_i32 s4, s4, s38
	buffer_load_dword v3, v28, s[20:23], s4 offen nt
	buffer_load_dwordx3 v[136:138], v27, s[24:27], s9 offen nt
	buffer_load_dword v4, v28, s[16:19], s7 offen nt
	buffer_load_dword v5, v28, s[16:19], s8 offen nt
	s_waitcnt vmcnt(8)
	s_add_i32 s4, s34, 9
	s_cmpk_lt_u32 s4, 0x201
	s_cselect_b64 s[12:13], s[40:41], 0
	v_cmp_eq_u32_e64 s[14:15], s37, v24
	s_and_b64 s[14:15], s[14:15], s[12:13]
	v_cndmask_b32_e64 v29, 0, 1, s[14:15]
	s_nop 1
	v_or_b32_dpp v56, v29, v29 wave_shr:1 row_mask:0xf bank_mask:0xf bound_ctrl:1
	s_nop 1
	v_or_b32_dpp v56, v29, v56 wave_shl:1 row_mask:0xf bank_mask:0xf bound_ctrl:1
	s_nop 1
	v_or_b32_dpp v78, v56, v56 wave_shr:1 row_mask:0xf bank_mask:0xf bound_ctrl:1
	s_nop 1
	v_or_b32_dpp v78, v56, v78 wave_shl:1 row_mask:0xf bank_mask:0xf bound_ctrl:1
	v_pk_add_f32 v[76:77], v[82:83], v[122:123]
	v_pk_add_f32 v[82:83], v[130:131], v[38:39]
	v_pk_add_f32 v[130:131], v[6:7], v[50:51]
	v_pk_add_f32 v[6:7], v[134:135], v[102:103]
	v_pk_fma_f32 v[82:83], v[108:109], v[76:77], v[82:83] op_sel_hi:[0,1,1] neg_lo:[1,0,0] neg_hi:[1,0,0]
	v_pk_fma_f32 v[130:131], v[108:109], v[76:77], v[130:131] op_sel:[1,0,0] neg_lo:[1,0,0] neg_hi:[1,0,0]
	v_pk_fma_f32 v[6:7], v[110:111], v[76:77], v[6:7] op_sel_hi:[0,1,1] neg_lo:[1,0,0] neg_hi:[1,0,0]
	v_pk_mul_f32 v[104:105], v[110:111], v[82:83] op_sel:[1,0]
	v_pk_mul_f32 v[120:121], v[112:113], v[82:83] op_sel_hi:[0,1]
	v_pk_mul_f32 v[128:129], v[112:113], v[82:83] op_sel:[1,0]
	v_pk_fma_f32 v[104:105], v[112:113], v[130:131], v[104:105] op_sel_hi:[0,1,1]
	v_pk_fma_f32 v[120:121], v[114:115], v[130:131], v[120:121] op_sel_hi:[0,1,1]
	v_pk_fma_f32 v[128:129], v[114:115], v[130:131], v[128:129] op_sel:[1,0,0]
	v_pk_fma_f32 v[104:105], v[112:113], v[6:7], v[104:105] op_sel:[1,0,0]
	v_pk_fma_f32 v[120:121], v[114:115], v[6:7], v[120:121] op_sel:[1,0,0]
	v_pk_fma_f32 v[128:129], v[116:117], v[6:7], v[128:129] op_sel_hi:[0,1,1]
	v_pk_mul_f32 v[134:135], v[108:109], v[104:105] op_sel_hi:[0,1]
	v_pk_fma_f32 v[134:135], v[108:109], v[120:121], v[134:135] op_sel:[1,0,0]
	v_pk_fma_f32 v[134:135], v[110:111], v[128:129], v[134:135] op_sel_hi:[0,1,1]
	v_pk_fma_f32 v[134:135], v[116:117], v[76:77], v[134:135] op_sel:[1,0,0] neg_lo:[0,0,1] neg_hi:[0,0,1]
	v_cmp_eq_u32_e64 s[10:11], 6, v119
	v_cmp_eq_u32_e64 s[14:15], 7, v119
	v_pk_add_f32 v[6:7], v[20:21], v[104:105]
	v_pk_add_f32 v[20:21], v[92:93], v[120:121]
	v_pk_add_f32 v[76:77], v[100:101], v[128:129]
	v_pk_add_f32 v[82:83], v[106:107], v[134:135]
	v_pk_fma_f32 v[106:107], v[12:13], v[6:7], v[82:83] op_sel_hi:[0,1,1]
	v_pk_fma_f32 v[130:131], v[64:65], v[6:7], v[82:83] op_sel_hi:[0,1,1]
	v_pk_fma_f32 v[106:107], v[12:13], v[20:21], v[106:107] op_sel:[1,0,0]
	v_pk_fma_f32 v[130:131], v[64:65], v[20:21], v[130:131] op_sel:[1,0,0]
	v_pk_fma_f32 v[106:107], v[14:15], v[76:77], v[106:107] op_sel_hi:[0,1,1]
	v_pk_fma_f32 v[130:131], v[66:67], v[76:77], v[130:131] op_sel_hi:[0,1,1]
	v_pk_fma_f32 v[82:83], v[172:173], v[6:7], v[82:83] op_sel_hi:[0,1,1]
	v_pk_fma_f32 v[82:83], v[172:173], v[20:21], v[82:83] op_sel:[1,0,0]
	v_pk_fma_f32 v[82:83], v[174:175], v[76:77], v[82:83] op_sel_hi:[0,1,1]
	v_cndmask_b32_e64 v92, 0, v18, s[10:11]
	v_cndmask_b32_e64 v93, 0, v18, s[14:15]
	v_add_f32_dpp v82, v106, v82 wave_shl:1 row_mask:0xf bank_mask:0xf bound_ctrl:1
	v_add_f32_dpp v83, v107, v83 wave_shl:1 row_mask:0xf bank_mask:0xf bound_ctrl:1
	s_add_i32 s4, s34, 5
	s_cmpk_lt_i32 s4, 0x201
	s_cselect_b64 s[12:13], s[0:1], 0
	v_add_f32_dpp v82, v130, v82 wave_shr:1 row_mask:0xf bank_mask:0xf bound_ctrl:1
	v_add_f32_dpp v83, v131, v83 wave_shr:1 row_mask:0xf bank_mask:0xf bound_ctrl:1
	v_pk_fma_f32 v[82:83], v[46:47], v[118:119], v[82:83] op_sel_hi:[1,0,1] neg_lo:[0,0,1] neg_hi:[0,0,1]
	v_pk_add_f32 v[82:83], v[82:83], v[92:93] neg_lo:[0,1] neg_hi:[0,1]
	v_pk_mul_f32 v[100:101], v[82:83], v[82:83]
	v_add_f32_e32 v100, v100, v101
	v_cndmask_b32_e64 v101, 0, v100, s[12:13]
	v_add_f32_e32 v1, v1, v101
	s_waitcnt vmcnt(8)
	v_mov_b32_dpp v12, v156 wave_shr:1 row_mask:0xf bank_mask:0xf bound_ctrl:1
	v_mov_b32_dpp v13, v157 wave_shr:1 row_mask:0xf bank_mask:0xf bound_ctrl:1
	v_mov_b32_dpp v14, v158 wave_shr:1 row_mask:0xf bank_mask:0xf bound_ctrl:1
	v_mov_b32_dpp v64, v156 wave_shl:1 row_mask:0xf bank_mask:0xf bound_ctrl:1
	v_mov_b32_dpp v65, v157 wave_shl:1 row_mask:0xf bank_mask:0xf bound_ctrl:1
	v_mov_b32_dpp v66, v158 wave_shl:1 row_mask:0xf bank_mask:0xf bound_ctrl:1
	v_pk_add_f32 v[6:7], v[156:157], v[12:13]
	v_pk_mul_f32 v[20:21], v[156:157], v[156:157] op_sel_hi:[0,1]
	v_pk_mul_f32 v[46:47], v[156:157], v[158:159] op_sel_hi:[1,0]
	v_mul_f32_e64 v76, v157, v157
	v_mul_f32_e64 v77, v158, v158
	v_add_f32_e64 v82, v158, v14
	v_pk_add_f32 v[6:7], v[6:7], v[64:65]
	v_or3_b32 v29, v78, v79, v57
	v_or3_b32 v29, v29, v58, v59
	s_add_i32 s4, s34, 6
	s_cmpk_lt_u32 s4, 0x1ff
	s_cselect_b64 s[12:13], s[42:43], 0
	v_cmp_ne_u32_e64 s[30:31], 0, v29
	s_and_b64 s[30:31], s[30:31], s[12:13]
	v_cndmask_b32_e64 v29, 0, 1.0, s[30:31]
	v_pk_fma_f32 v[20:21], v[12:13], v[12:13], v[20:21] op_sel_hi:[0,1,1]
	v_pk_fma_f32 v[46:47], v[12:13], v[14:15], v[46:47] op_sel_hi:[1,0,1]
	v_fma_f32 v76, v13, v13, v76
	v_fma_f32 v77, v14, v14, v77
	v_add_f32_dpp v83, v29, v29 wave_shr:1 row_mask:0xf bank_mask:0xf bound_ctrl:1
	v_add_f32_e64 v82, v82, v66
	v_pk_fma_f32 v[20:21], v[64:65], v[64:65], v[20:21] op_sel_hi:[0,1,1]
	v_pk_fma_f32 v[46:47], v[64:65], v[66:67], v[46:47] op_sel_hi:[1,0,1]
	v_fma_f32 v76, v65, v65, v76
	v_fma_f32 v77, v66, v66, v77
	v_add_f32_dpp v83, v29, v83 wave_shl:1 row_mask:0xf bank_mask:0xf bound_ctrl:1
	v_pk_add_f32 v[92:93], v[36:37], v[6:7]
	v_pk_add_f32 v[100:101], v[54:55], v[92:93]
	v_pk_add_f32 v[36:37], v[60:61], v[20:21]
	v_pk_add_f32 v[54:55], v[70:71], v[36:37]
	v_pk_add_f32 v[60:61], v[68:69], v[46:47]
	v_pk_add_f32 v[70:71], v[74:75], v[60:61]
	v_pk_add_f32 v[74:75], v[94:95], v[76:77]
	v_pk_add_f32 v[68:69], v[88:89], v[74:75]
	v_pk_add_f32 v[88:89], v[98:99], v[82:83]
	v_pk_add_f32 v[94:95], v[90:91], v[88:89]
	v_mul_f32_e64 v108, v100, v22
	v_mul_f32_e64 v109, v101, v22
	v_mul_f32_e64 v110, v94, v22
	v_fma_f32 v29, v54, v22, v26
	v_mul_f32_e64 v56, v55, v22
	v_mul_f32_e64 v90, v70, v22
	v_fma_f32 v91, v68, v22, v26
	v_mul_f32_e64 v98, v71, v22
	v_fma_f32 v99, v69, v22, v26
	v_fma_f32 v29, -v108, v108, v29
	v_fma_f32 v56, -v108, v109, v56
	v_fma_f32 v90, -v108, v110, v90
	v_fma_f32 v91, -v109, v109, v91
	v_fma_f32 v98, -v109, v110, v98
	v_fma_f32 v99, -v110, v110, v99
	v_mul_f32_e64 v106, v98, v98
	v_mul_f32_e64 v107, v56, v99
	v_mul_f32_e64 v130, v90, v91
	v_mul_f32_e64 v131, v90, v90
	v_mul_f32_e64 v140, v29, v98
	v_mul_f32_e64 v141, v56, v56
	v_fma_f32 v106, v91, v99, -v106
	v_fma_f32 v107, v90, v98, -v107
	v_fma_f32 v130, v56, v98, -v130
	v_fma_f32 v131, v29, v99, -v131
	v_fma_f32 v140, v56, v90, -v140
	v_fma_f32 v141, v29, v91, -v141
	v_mul_f32_e64 v144, v29, v106
	v_fma_f32 v144, v56, v107, v144
	v_fma_f32 v144, v90, v130, v144
	v_rcp_f32_e32 v144, v144
	v_cmp_ne_u32_e64 vcc, s37, v16
	v_mul_f32_e64 v144, v144, v22
	v_cndmask_b32_e64 v144, 0, v144, s[30:31]
	v_cndmask_b32_e64 v29, 0, v18, vcc
	v_cndmask_b32_e64 v117, 0, v22, s[30:31]
	v_mul_f32_e64 v111, v106, v144
	v_mul_f32_e64 v112, v107, v144
	v_mul_f32_e64 v113, v130, v144
	v_mul_f32_e64 v114, v131, v144
	v_mul_f32_e64 v115, v140, v144
	v_mul_f32_e64 v116, v141, v144
	v_add_f32_e64 v118, v95, v29
	v_mov_b32_e32 v119, v16
	ds_write_b128 v23, v[108:111]
	ds_write_b128 v23, v[112:115] offset:1024
	ds_write_b128 v23, v[116:119] offset:2048
	v_mov_b32_dpp v54, v52 wave_shr:1 row_mask:0xf bank_mask:0xf bound_ctrl:1
	v_mov_b32_dpp v55, v53 wave_shr:1 row_mask:0xf bank_mask:0xf bound_ctrl:1
	v_mov_b32_dpp v70, v52 wave_shl:1 row_mask:0xf bank_mask:0xf bound_ctrl:1
	v_mov_b32_dpp v71, v53 wave_shl:1 row_mask:0xf bank_mask:0xf bound_ctrl:1
	v_pk_mul_f32 v[68:69], v[52:53], v[156:157] op_sel_hi:[1,0]
	v_pk_mul_f32 v[100:101], v[52:53], v[156:157] op_sel:[0,1]
	v_pk_mul_f32 v[140:141], v[52:53], v[158:159] op_sel_hi:[1,0]
	v_pk_add_f32 v[144:145], v[52:53], v[54:55]
	v_pk_fma_f32 v[68:69], v[54:55], v[12:13], v[68:69] op_sel_hi:[1,0,1]
	v_pk_fma_f32 v[100:101], v[54:55], v[12:13], v[100:101] op_sel:[0,1,0]
	v_pk_fma_f32 v[140:141], v[54:55], v[14:15], v[140:141] op_sel_hi:[1,0,1]
	v_pk_add_f32 v[144:145], v[144:145], v[70:71]
	v_pk_fma_f32 v[68:69], v[70:71], v[64:65], v[68:69] op_sel_hi:[1,0,1]
	v_pk_fma_f32 v[100:101], v[70:71], v[64:65], v[100:101] op_sel:[0,1,0]
	v_pk_fma_f32 v[140:141], v[70:71], v[66:67], v[140:141] op_sel_hi:[1,0,1]
	s_waitcnt lgkmcnt(0)
	s_barrier
	s_add_i32 s5, s34, 11
	s_min_i32 s5, s5, 0x200
	s_mul_i32 s6, s5, 0x804
	s_add_i32 s6, s6, s35
	s_add_i32 s7, s6, 0x505014
	s_add_i32 s8, s6, 0x606018
	s_mul_i32 s9, s5, 0x180c
	s_add_i32 s9, s9, s33
	s_add_i32 s4, s34, 12
	s_min_i32 s4, s4, 0x200
	s_mul_i32 s4, s4, 0x804
	s_add_i32 s4, s4, s38
	buffer_load_dword v16, v28, s[20:23], s4 offen nt
	buffer_load_dwordx3 v[160:162], v27, s[24:27], s9 offen nt
	buffer_load_dword v54, v28, s[16:19], s7 offen nt
	buffer_load_dword v55, v28, s[16:19], s8 offen nt
	s_waitcnt vmcnt(8)
	s_add_i32 s4, s34, 10
	s_cmpk_lt_u32 s4, 0x201
	s_cselect_b64 s[12:13], s[40:41], 0
	v_cmp_eq_u32_e64 s[14:15], s37, v2
	s_and_b64 s[14:15], s[14:15], s[12:13]
	v_cndmask_b32_e64 v29, 0, 1, s[14:15]
	s_nop 1
	v_or_b32_dpp v56, v29, v29 wave_shr:1 row_mask:0xf bank_mask:0xf bound_ctrl:1
	s_nop 1
	v_or_b32_dpp v56, v29, v56 wave_shl:1 row_mask:0xf bank_mask:0xf bound_ctrl:1
	s_nop 1
	v_or_b32_dpp v59, v56, v56 wave_shr:1 row_mask:0xf bank_mask:0xf bound_ctrl:1
	s_nop 1
	v_or_b32_dpp v59, v56, v59 wave_shl:1 row_mask:0xf bank_mask:0xf bound_ctrl:1
	v_pk_add_f32 v[70:71], v[122:123], v[144:145]
	v_pk_add_f32 v[90:91], v[80:81], v[70:71]
	v_pk_add_f32 v[94:95], v[38:39], v[68:69]
	v_pk_add_f32 v[80:81], v[44:45], v[94:95]
	v_pk_add_f32 v[38:39], v[50:51], v[100:101]
	v_pk_add_f32 v[44:45], v[48:49], v[38:39]
	v_pk_add_f32 v[50:51], v[102:103], v[140:141]
	v_pk_add_f32 v[48:49], v[72:73], v[50:51]
	v_pk_fma_f32 v[80:81], v[108:109], v[90:91], v[80:81] op_sel_hi:[0,1,1] neg_lo:[1,0,0] neg_hi:[1,0,0]
	v_pk_fma_f32 v[44:45], v[108:109], v[90:91], v[44:45] op_sel:[1,0,0] neg_lo:[1,0,0] neg_hi:[1,0,0]
	v_pk_fma_f32 v[48:49], v[110:111], v[90:91], v[48:49] op_sel_hi:[0,1,1] neg_lo:[1,0,0] neg_hi:[1,0,0]
	v_pk_mul_f32 v[98:99], v[110:111], v[80:81] op_sel:[1,0]
	v_pk_mul_f32 v[102:103], v[112:113], v[80:81] op_sel_hi:[0,1]
	v_pk_mul_f32 v[106:107], v[112:113], v[80:81] op_sel:[1,0]
	v_pk_fma_f32 v[98:99], v[112:113], v[44:45], v[98:99] op_sel_hi:[0,1,1]
	v_pk_fma_f32 v[102:103], v[114:115], v[44:45], v[102:103] op_sel_hi:[0,1,1]
	v_pk_fma_f32 v[106:107], v[114:115], v[44:45], v[106:107] op_sel:[1,0,0]
	v_pk_fma_f32 v[98:99], v[112:113], v[48:49], v[98:99] op_sel:[1,0,0]
	v_pk_fma_f32 v[102:103], v[114:115], v[48:49], v[102:103] op_sel:[1,0,0]
	v_pk_fma_f32 v[106:107], v[116:117], v[48:49], v[106:107] op_sel_hi:[0,1,1]
	v_pk_mul_f32 v[72:73], v[108:109], v[98:99] op_sel_hi:[0,1]
	v_pk_fma_f32 v[72:73], v[108:109], v[102:103], v[72:73] op_sel:[1,0,0]
	v_pk_fma_f32 v[72:73], v[110:111], v[106:107], v[72:73] op_sel_hi:[0,1,1]
	v_pk_fma_f32 v[72:73], v[116:117], v[90:91], v[72:73] op_sel:[1,0,0] neg_lo:[0,0,1] neg_hi:[0,0,1]
	v_cmp_eq_u32_e64 s[10:11], 6, v119
	v_cmp_eq_u32_e64 s[14:15], 7, v119
	v_pk_add_f32 v[44:45], v[104:105], v[98:99]
	v_pk_add_f32 v[48:49], v[142:143], v[44:45]
	v_pk_add_f32 v[80:81], v[120:121], v[102:103]
	v_pk_add_f32 v[90:91], v[146:147], v[80:81]
	v_pk_add_f32 v[104:105], v[128:129], v[106:107]
	v_pk_add_f32 v[120:121], v[154:155], v[104:105]
	v_pk_add_f32 v[122:123], v[134:135], v[72:73]
	v_pk_add_f32 v[130:131], v[132:133], v[122:123]
	v_pk_fma_f32 v[134:135], v[32:33], v[48:49], v[130:131] op_sel_hi:[0,1,1]
	v_pk_fma_f32 v[142:143], v[84:85], v[48:49], v[130:131] op_sel_hi:[0,1,1]
	v_pk_fma_f32 v[134:135], v[32:33], v[90:91], v[134:135] op_sel:[1,0,0]
	v_pk_fma_f32 v[142:143], v[84:85], v[90:91], v[142:143] op_sel:[1,0,0]
	v_pk_fma_f32 v[134:135], v[34:35], v[120:121], v[134:135] op_sel_hi:[0,1,1]
	v_pk_fma_f32 v[142:143], v[86:87], v[120:121], v[142:143] op_sel_hi:[0,1,1]
	v_pk_fma_f32 v[130:131], v[148:149], v[48:49], v[130:131] op_sel_hi:[0,1,1]
	v_pk_fma_f32 v[130:131], v[148:149], v[90:91], v[130:131] op_sel:[1,0,0]
	v_pk_fma_f32 v[130:131], v[150:151], v[120:121], v[130:131] op_sel_hi:[0,1,1]
	v_cndmask_b32_e64 v128, 0, v18, s[10:11]
	v_cndmask_b32_e64 v129, 0, v18, s[14:15]
	v_add_f32_dpp v130, v134, v130 wave_shl:1 row_mask:0xf bank_mask:0xf bound_ctrl:1
	v_add_f32_dpp v131, v135, v131 wave_shl:1 row_mask:0xf bank_mask:0xf bound_ctrl:1
	s_add_i32 s4, s34, 6
	s_cmpk_lt_i32 s4, 0x201
	s_cselect_b64 s[12:13], s[0:1], 0
	v_add_f32_dpp v130, v142, v130 wave_shr:1 row_mask:0xf bank_mask:0xf bound_ctrl:1
	v_add_f32_dpp v131, v143, v131 wave_shr:1 row_mask:0xf bank_mask:0xf bound_ctrl:1
	v_pk_fma_f32 v[130:131], v[96:97], v[118:119], v[130:131] op_sel_hi:[1,0,1] neg_lo:[0,0,1] neg_hi:[0,0,1]
	v_pk_add_f32 v[130:131], v[130:131], v[128:129] neg_lo:[0,1] neg_hi:[0,1]
	v_pk_mul_f32 v[132:133], v[130:131], v[130:131]
	v_add_f32_e32 v132, v132, v133
	v_cndmask_b32_e64 v133, 0, v132, s[12:13]
	v_add_f32_e32 v1, v1, v133
	s_waitcnt vmcnt(8)
	v_mov_b32_dpp v32, v124 wave_shr:1 row_mask:0xf bank_mask:0xf bound_ctrl:1
	v_mov_b32_dpp v33, v125 wave_shr:1 row_mask:0xf bank_mask:0xf bound_ctrl:1
	v_mov_b32_dpp v34, v126 wave_shr:1 row_mask:0xf bank_mask:0xf bound_ctrl:1
	v_mov_b32_dpp v84, v124 wave_shl:1 row_mask:0xf bank_mask:0xf bound_ctrl:1
	v_mov_b32_dpp v85, v125 wave_shl:1 row_mask:0xf bank_mask:0xf bound_ctrl:1
	v_mov_b32_dpp v86, v126 wave_shl:1 row_mask:0xf bank_mask:0xf bound_ctrl:1
	v_pk_add_f32 v[48:49], v[124:125], v[32:33]
	v_pk_mul_f32 v[90:91], v[124:125], v[124:125] op_sel_hi:[0,1]
	v_pk_mul_f32 v[96:97], v[124:125], v[126:127] op_sel_hi:[1,0]
	v_mul_f32_e64 v108, v125, v125
	v_mul_f32_e64 v109, v126, v126
	v_add_f32_e64 v110, v126, v34
	v_pk_add_f32 v[48:49], v[48:49], v[84:85]
	v_or3_b32 v29, v59, v78, v79
	v_or3_b32 v29, v29, v57, v58
	s_add_i32 s4, s34, 7
	s_cmpk_lt_u32 s4, 0x1ff
	s_cselect_b64 s[12:13], s[42:43], 0
	v_cmp_ne_u32_e64 s[30:31], 0, v29
	s_and_b64 s[30:31], s[30:31], s[12:13]
	v_cndmask_b32_e64 v29, 0, 1.0, s[30:31]
	v_pk_fma_f32 v[90:91], v[32:33], v[32:33], v[90:91] op_sel_hi:[0,1,1]
	v_pk_fma_f32 v[96:97], v[32:33], v[34:35], v[96:97] op_sel_hi:[1,0,1]
	v_fma_f32 v108, v33, v33, v108
	v_fma_f32 v109, v34, v34, v109
	v_add_f32_dpp v111, v29, v29 wave_shr:1 row_mask:0xf bank_mask:0xf bound_ctrl:1
	v_add_f32_e64 v110, v110, v86
	v_pk_fma_f32 v[90:91], v[84:85], v[84:85], v[90:91] op_sel_hi:[0,1,1]
	v_pk_fma_f32 v[96:97], v[84:85], v[86:87], v[96:97] op_sel_hi:[1,0,1]
	v_fma_f32 v108, v85, v85, v108
	v_fma_f32 v109, v86, v86, v109
	v_add_f32_dpp v111, v29, v111 wave_shl:1 row_mask:0xf bank_mask:0xf bound_ctrl:1
	v_pk_add_f32 v[112:113], v[92:93], v[48:49]
	v_pk_add_f32 v[92:93], v[36:37], v[90:91]
	v_pk_add_f32 v[36:37], v[60:61], v[96:97]
	v_pk_add_f32 v[60:61], v[74:75], v[108:109]
	v_pk_add_f32 v[74:75], v[88:89], v[110:111]
	v_mul_f32_e64 v116, v112, v22
	v_mul_f32_e64 v117, v113, v22
	v_mul_f32_e64 v118, v74, v22
	v_fma_f32 v29, v92, v22, v26
	v_mul_f32_e64 v56, v93, v22
	v_mul_f32_e64 v88, v36, v22
	v_fma_f32 v89, v60, v22, v26
	v_mul_f32_e64 v114, v37, v22
	v_fma_f32 v115, v61, v22, v26
	v_fma_f32 v29, -v116, v116, v29
	v_fma_f32 v56, -v116, v117, v56
	v_fma_f32 v88, -v116, v118, v88
	v_fma_f32 v89, -v117, v117, v89
	v_fma_f32 v114, -v117, v118, v114
	v_fma_f32 v115, -v118, v118, v115
	v_mul_f32_e64 v120, v114, v114
	v_mul_f32_e64 v121, v56, v115
	v_mul_f32_e64 v142, v88, v89
	v_mul_f32_e64 v143, v88, v88
	v_mul_f32_e64 v146, v29, v114
	v_mul_f32_e64 v147, v56, v56
	v_fma_f32 v120, v89, v115, -v120
	v_fma_f32 v121, v88, v114, -v121
	v_fma_f32 v142, v56, v114, -v142
	v_fma_f32 v143, v29, v115, -v143
	v_fma_f32 v146, v56, v88, -v146
	v_fma_f32 v147, v29, v89, -v147
	v_mul_f32_e64 v148, v29, v120
	v_fma_f32 v148, v56, v121, v148
	v_fma_f32 v148, v88, v142, v148
	v_rcp_f32_e32 v148, v148
	v_cmp_ne_u32_e64 vcc, s37, v17
	v_mul_f32_e64 v148, v148, v22
	v_cndmask_b32_e64 v148, 0, v148, s[30:31]
	v_cndmask_b32_e64 v29, 0, v18, vcc
	v_cndmask_b32_e64 v133, 0, v22, s[30:31]
	v_mul_f32_e64 v119, v120, v148
	v_mul_f32_e64 v128, v121, v148
	v_mul_f32_e64 v129, v142, v148
	v_mul_f32_e64 v130, v143, v148
	v_mul_f32_e64 v131, v146, v148
	v_mul_f32_e64 v132, v147, v148
	v_add_f32_e64 v134, v75, v29
	v_mov_b32_e32 v135, v17
	ds_write_b128 v23, v[116:119] offset:3072
	ds_write_b128 v23, v[128:131] offset:4096
	ds_write_b128 v23, v[132:135] offset:5120
	v_mov_b32_dpp v36, v30 wave_shr:1 row_mask:0xf bank_mask:0xf bound_ctrl:1
	v_mov_b32_dpp v37, v31 wave_shr:1 row_mask:0xf bank_mask:0xf bound_ctrl:1
	v_mov_b32_dpp v60, v30 wave_shl:1 row_mask:0xf bank_mask:0xf bound_ctrl:1
	v_mov_b32_dpp v61, v31 wave_shl:1 row_mask:0xf bank_mask:0xf bound_ctrl:1
	v_pk_mul_f32 v[74:75], v[30:31], v[124:125] op_sel_hi:[1,0]
	v_pk_mul_f32 v[114:115], v[30:31], v[124:125] op_sel:[0,1]
	v_pk_mul_f32 v[142:143], v[30:31], v[126:127] op_sel_hi:[1,0]
	v_pk_add_f32 v[146:147], v[30:31], v[36:37]
	v_pk_fma_f32 v[74:75], v[36:37], v[32:33], v[74:75] op_sel_hi:[1,0,1]
	v_pk_fma_f32 v[114:115], v[36:37], v[32:33], v[114:115] op_sel:[0,1,0]
	v_pk_fma_f32 v[142:143], v[36:37], v[34:35], v[142:143] op_sel_hi:[1,0,1]
	v_pk_add_f32 v[146:147], v[146:147], v[60:61]
	v_pk_fma_f32 v[74:75], v[60:61], v[84:85], v[74:75] op_sel_hi:[1,0,1]
	v_pk_fma_f32 v[114:115], v[60:61], v[84:85], v[114:115] op_sel:[0,1,0]
	v_pk_fma_f32 v[142:143], v[60:61], v[86:87], v[142:143] op_sel_hi:[1,0,1]
	s_waitcnt lgkmcnt(0)
	s_barrier
	s_waitcnt vmcnt(4)
	s_add_i32 s4, s34, 11
	s_cmpk_lt_u32 s4, 0x201
	s_cselect_b64 s[12:13], s[40:41], 0
	v_cmp_eq_u32_e64 s[14:15], s37, v3
	s_and_b64 s[14:15], s[14:15], s[12:13]
	v_cndmask_b32_e64 v17, 0, 1, s[14:15]
	s_nop 1
	v_or_b32_dpp v29, v17, v17 wave_shr:1 row_mask:0xf bank_mask:0xf bound_ctrl:1
	s_nop 1
	v_or_b32_dpp v29, v17, v29 wave_shl:1 row_mask:0xf bank_mask:0xf bound_ctrl:1
	s_nop 1
	v_or_b32_dpp v56, v29, v29 wave_shr:1 row_mask:0xf bank_mask:0xf bound_ctrl:1
	s_nop 1
	v_or_b32_dpp v56, v29, v56 wave_shl:1 row_mask:0xf bank_mask:0xf bound_ctrl:1
	v_pk_add_f32 v[36:37], v[70:71], v[146:147]
	v_pk_add_f32 v[70:71], v[94:95], v[74:75]
	v_pk_add_f32 v[94:95], v[38:39], v[114:115]
	v_pk_add_f32 v[38:39], v[50:51], v[142:143]
	v_pk_fma_f32 v[70:71], v[116:117], v[36:37], v[70:71] op_sel_hi:[0,1,1] neg_lo:[1,0,0] neg_hi:[1,0,0]
	v_pk_fma_f32 v[94:95], v[116:117], v[36:37], v[94:95] op_sel:[1,0,0] neg_lo:[1,0,0] neg_hi:[1,0,0]
	v_pk_fma_f32 v[38:39], v[118:119], v[36:37], v[38:39] op_sel_hi:[0,1,1] neg_lo:[1,0,0] neg_hi:[1,0,0]
	v_pk_mul_f32 v[60:61], v[118:119], v[70:71] op_sel:[1,0]
	v_pk_mul_f32 v[88:89], v[128:129], v[70:71] op_sel_hi:[0,1]
	v_pk_mul_f32 v[92:93], v[128:129], v[70:71] op_sel:[1,0]
	v_pk_fma_f32 v[60:61], v[128:129], v[94:95], v[60:61] op_sel_hi:[0,1,1]
	v_pk_fma_f32 v[88:89], v[130:131], v[94:95], v[88:89] op_sel_hi:[0,1,1]
	v_pk_fma_f32 v[92:93], v[130:131], v[94:95], v[92:93] op_sel:[1,0,0]
	v_pk_fma_f32 v[60:61], v[128:129], v[38:39], v[60:61] op_sel:[1,0,0]
	v_pk_fma_f32 v[88:89], v[130:131], v[38:39], v[88:89] op_sel:[1,0,0]
	v_pk_fma_f32 v[92:93], v[132:133], v[38:39], v[92:93] op_sel_hi:[0,1,1]
	v_pk_mul_f32 v[50:51], v[116:117], v[60:61] op_sel_hi:[0,1]
	v_pk_fma_f32 v[50:51], v[116:117], v[88:89], v[50:51] op_sel:[1,0,0]
	v_pk_fma_f32 v[50:51], v[118:119], v[92:93], v[50:51] op_sel_hi:[0,1,1]
	v_pk_fma_f32 v[50:51], v[132:133], v[36:37], v[50:51] op_sel:[1,0,0] neg_lo:[0,0,1] neg_hi:[0,0,1]
	v_cmp_eq_u32_e64 s[10:11], 6, v135
	v_cmp_eq_u32_e64 s[14:15], 7, v135
	v_pk_add_f32 v[36:37], v[44:45], v[60:61]
	v_pk_add_f32 v[38:39], v[80:81], v[88:89]
	v_pk_add_f32 v[44:45], v[104:105], v[92:93]
	v_pk_add_f32 v[70:71], v[122:123], v[50:51]
	v_pk_fma_f32 v[94:95], v[8:9], v[36:37], v[70:71] op_sel_hi:[0,1,1]
	v_pk_fma_f32 v[122:123], v[40:41], v[36:37], v[70:71] op_sel_hi:[0,1,1]
	v_pk_fma_f32 v[94:95], v[8:9], v[38:39], v[94:95] op_sel:[1,0,0]
	v_pk_fma_f32 v[122:123], v[40:41], v[38:39], v[122:123] op_sel:[1,0,0]
	v_pk_fma_f32 v[94:95], v[10:11], v[44:45], v[94:95] op_sel_hi:[0,1,1]
	v_pk_fma_f32 v[122:123], v[42:43], v[44:45], v[122:123] op_sel_hi:[0,1,1]
	v_pk_fma_f32 v[70:71], v[168:169], v[36:37], v[70:71] op_sel_hi:[0,1,1]
	v_pk_fma_f32 v[70:71], v[168:169], v[38:39], v[70:71] op_sel:[1,0,0]
	v_pk_fma_f32 v[70:71], v[170:171], v[44:45], v[70:71] op_sel_hi:[0,1,1]
	v_cndmask_b32_e64 v80, 0, v18, s[10:11]
	v_cndmask_b32_e64 v81, 0, v18, s[14:15]
	v_add_f32_dpp v70, v94, v70 wave_shl:1 row_mask:0xf bank_mask:0xf bound_ctrl:1
	v_add_f32_dpp v71, v95, v71 wave_shl:1 row_mask:0xf bank_mask:0xf bound_ctrl:1
	s_add_i32 s4, s34, 7
	s_cmpk_lt_i32 s4, 0x201
	s_cselect_b64 s[12:13], s[0:1], 0
	v_add_f32_dpp v70, v122, v70 wave_shr:1 row_mask:0xf bank_mask:0xf bound_ctrl:1
	v_add_f32_dpp v71, v123, v71 wave_shr:1 row_mask:0xf bank_mask:0xf bound_ctrl:1
	v_pk_fma_f32 v[70:71], v[62:63], v[134:135], v[70:71] op_sel_hi:[1,0,1] neg_lo:[0,0,1] neg_hi:[0,0,1]
	v_pk_add_f32 v[70:71], v[70:71], v[80:81] neg_lo:[0,1] neg_hi:[0,1]
	v_pk_mul_f32 v[104:105], v[70:71], v[70:71]
	v_add_f32_e32 v104, v104, v105
	v_cndmask_b32_e64 v105, 0, v104, s[12:13]
	v_add_f32_e32 v1, v1, v105
	s_waitcnt vmcnt(4)
	v_mov_b32_dpp v8, v136 wave_shr:1 row_mask:0xf bank_mask:0xf bound_ctrl:1
	v_mov_b32_dpp v9, v137 wave_shr:1 row_mask:0xf bank_mask:0xf bound_ctrl:1
	v_mov_b32_dpp v10, v138 wave_shr:1 row_mask:0xf bank_mask:0xf bound_ctrl:1
	v_mov_b32_dpp v36, v136 wave_shl:1 row_mask:0xf bank_mask:0xf bound_ctrl:1
	v_mov_b32_dpp v37, v137 wave_shl:1 row_mask:0xf bank_mask:0xf bound_ctrl:1
	v_mov_b32_dpp v38, v138 wave_shl:1 row_mask:0xf bank_mask:0xf bound_ctrl:1
	v_pk_add_f32 v[40:41], v[136:137], v[8:9]
	v_pk_mul_f32 v[42:43], v[136:137], v[136:137] op_sel_hi:[0,1]
	v_pk_mul_f32 v[44:45], v[136:137], v[138:139] op_sel_hi:[1,0]
	v_mul_f32_e64 v62, v137, v137
	v_mul_f32_e64 v63, v138, v138
	v_add_f32_e64 v70, v138, v10
	v_pk_add_f32 v[40:41], v[40:41], v[36:37]
	v_or3_b32 v17, v56, v59, v78
	v_or3_b32 v17, v17, v79, v57
	s_add_i32 s4, s34, 8
	s_cmpk_lt_u32 s4, 0x1ff
	s_cselect_b64 s[12:13], s[42:43], 0
	v_cmp_ne_u32_e64 s[30:31], 0, v17
	s_and_b64 s[30:31], s[30:31], s[12:13]
	v_cndmask_b32_e64 v17, 0, 1.0, s[30:31]
	v_pk_fma_f32 v[42:43], v[8:9], v[8:9], v[42:43] op_sel_hi:[0,1,1]
	v_pk_fma_f32 v[44:45], v[8:9], v[10:11], v[44:45] op_sel_hi:[1,0,1]
	v_fma_f32 v62, v9, v9, v62
	v_fma_f32 v63, v10, v10, v63
	v_add_f32_dpp v71, v17, v17 wave_shr:1 row_mask:0xf bank_mask:0xf bound_ctrl:1
	v_add_f32_e64 v70, v70, v38
	v_pk_fma_f32 v[42:43], v[36:37], v[36:37], v[42:43] op_sel_hi:[0,1,1]
	v_pk_fma_f32 v[44:45], v[36:37], v[38:39], v[44:45] op_sel_hi:[1,0,1]
	v_fma_f32 v62, v37, v37, v62
	v_fma_f32 v63, v38, v38, v63
	v_add_f32_dpp v71, v17, v71 wave_shl:1 row_mask:0xf bank_mask:0xf bound_ctrl:1
	v_pk_add_f32 v[80:81], v[48:49], v[40:41]
	v_pk_add_f32 v[94:95], v[6:7], v[80:81]
	v_pk_add_f32 v[6:7], v[90:91], v[42:43]
	v_pk_add_f32 v[48:49], v[20:21], v[6:7]
	v_pk_add_f32 v[20:21], v[96:97], v[44:45]
	v_pk_add_f32 v[90:91], v[46:47], v[20:21]
	v_pk_add_f32 v[46:47], v[108:109], v[62:63]
	v_pk_add_f32 v[96:97], v[76:77], v[46:47]
	v_pk_add_f32 v[76:77], v[110:111], v[70:71]
	v_pk_add_f32 v[104:105], v[82:83], v[76:77]
	v_mul_f32_e64 v108, v94, v22
	v_mul_f32_e64 v109, v95, v22
	v_mul_f32_e64 v110, v104, v22
	v_fma_f32 v17, v48, v22, v26
	v_mul_f32_e64 v29, v49, v22
	v_mul_f32_e64 v58, v90, v22
	v_fma_f32 v82, v96, v22, v26
	v_mul_f32_e64 v83, v91, v22
	v_fma_f32 v112, v97, v22, v26
	v_fma_f32 v17, -v108, v108, v17
	v_fma_f32 v29, -v108, v109, v29
	v_fma_f32 v58, -v108, v110, v58
	v_fma_f32 v82, -v109, v109, v82
	v_fma_f32 v83, -v109, v110, v83
	v_fma_f32 v112, -v110, v110, v112
	v_mul_f32_e64 v113, v83, v83
	v_mul_f32_e64 v128, v29, v112
	v_mul_f32_e64 v129, v58, v82
	v_mul_f32_e64 v130, v58, v58
	v_mul_f32_e64 v131, v17, v83
	v_mul_f32_e64 v132, v29, v29
	v_fma_f32 v113, v82, v112, -v113
	v_fma_f32 v128, v58, v83, -v128
	v_fma_f32 v129, v29, v83, -v129
	v_fma_f32 v130, v17, v112, -v130
	v_fma_f32 v131, v29, v58, -v131
	v_fma_f32 v132, v17, v82, -v132
	v_mul_f32_e64 v133, v17, v113
	v_fma_f32 v133, v29, v128, v133
	v_fma_f32 v133, v58, v129, v133
	v_rcp_f32_e32 v133, v133
	v_cmp_ne_u32_e64 vcc, s37, v25
	v_mul_f32_e64 v133, v133, v22
	v_cndmask_b32_e64 v133, 0, v133, s[30:31]
	v_cndmask_b32_e64 v17, 0, v18, vcc
	v_cndmask_b32_e64 v121, 0, v22, s[30:31]
	v_mul_f32_e64 v111, v113, v133
	v_mul_f32_e64 v116, v128, v133
	v_mul_f32_e64 v117, v129, v133
	v_mul_f32_e64 v118, v130, v133
	v_mul_f32_e64 v119, v131, v133
	v_mul_f32_e64 v120, v132, v133
	v_add_f32_e64 v122, v105, v17
	v_mov_b32_e32 v123, v25
	ds_write_b128 v23, v[108:111]
	ds_write_b128 v23, v[116:119] offset:1024
	ds_write_b128 v23, v[120:123] offset:2048
	v_mov_b32_dpp v82, v4 wave_shr:1 row_mask:0xf bank_mask:0xf bound_ctrl:1
	v_mov_b32_dpp v83, v5 wave_shr:1 row_mask:0xf bank_mask:0xf bound_ctrl:1
	v_mov_b32_dpp v90, v4 wave_shl:1 row_mask:0xf bank_mask:0xf bound_ctrl:1
	v_mov_b32_dpp v91, v5 wave_shl:1 row_mask:0xf bank_mask:0xf bound_ctrl:1
	v_pk_mul_f32 v[48:49], v[4:5], v[136:137] op_sel_hi:[1,0]
	v_pk_mul_f32 v[96:97], v[4:5], v[136:137] op_sel:[0,1]
	v_pk_mul_f32 v[104:105], v[4:5], v[138:139] op_sel_hi:[1,0]
	v_pk_add_f32 v[112:113], v[4:5], v[82:83]
	v_pk_fma_f32 v[48:49], v[82:83], v[8:9], v[48:49] op_sel_hi:[1,0,1]
	v_pk_fma_f32 v[96:97], v[82:83], v[8:9], v[96:97] op_sel:[0,1,0]
	v_pk_fma_f32 v[104:105], v[82:83], v[10:11], v[104:105] op_sel_hi:[1,0,1]
	v_pk_add_f32 v[112:113], v[112:113], v[90:91]
	v_pk_fma_f32 v[48:49], v[90:91], v[36:37], v[48:49] op_sel_hi:[1,0,1]
	v_pk_fma_f32 v[96:97], v[90:91], v[36:37], v[96:97] op_sel:[0,1,0]
	v_pk_fma_f32 v[104:105], v[90:91], v[38:39], v[104:105] op_sel_hi:[1,0,1]
	s_waitcnt lgkmcnt(0)
	s_barrier
	s_waitcnt vmcnt(0)
	s_add_i32 s4, s34, 12
	s_cmpk_lt_u32 s4, 0x201
	s_cselect_b64 s[12:13], s[40:41], 0
	v_cmp_eq_u32_e64 s[14:15], s37, v16
	s_and_b64 s[14:15], s[14:15], s[12:13]
	v_cndmask_b32_e64 v17, 0, 1, s[14:15]
	s_nop 1
	v_or_b32_dpp v25, v17, v17 wave_shr:1 row_mask:0xf bank_mask:0xf bound_ctrl:1
	s_nop 1
	v_or_b32_dpp v25, v17, v25 wave_shl:1 row_mask:0xf bank_mask:0xf bound_ctrl:1
	s_nop 1
	v_or_b32_dpp v29, v25, v25 wave_shr:1 row_mask:0xf bank_mask:0xf bound_ctrl:1
	s_nop 1
	v_or_b32_dpp v29, v25, v29 wave_shl:1 row_mask:0xf bank_mask:0xf bound_ctrl:1
	v_pk_add_f32 v[82:83], v[146:147], v[112:113]
	v_pk_add_f32 v[90:91], v[144:145], v[82:83]
	v_pk_add_f32 v[94:95], v[74:75], v[48:49]
	v_pk_add_f32 v[128:129], v[68:69], v[94:95]
	v_pk_add_f32 v[74:75], v[114:115], v[96:97]
	v_pk_add_f32 v[68:69], v[100:101], v[74:75]
	v_pk_add_f32 v[114:115], v[142:143], v[104:105]
	v_pk_add_f32 v[100:101], v[140:141], v[114:115]
	v_pk_fma_f32 v[128:129], v[108:109], v[90:91], v[128:129] op_sel_hi:[0,1,1] neg_lo:[1,0,0] neg_hi:[1,0,0]
	v_pk_fma_f32 v[68:69], v[108:109], v[90:91], v[68:69] op_sel:[1,0,0] neg_lo:[1,0,0] neg_hi:[1,0,0]
	v_pk_fma_f32 v[100:101], v[110:111], v[90:91], v[100:101] op_sel_hi:[0,1,1] neg_lo:[1,0,0] neg_hi:[1,0,0]
	v_pk_mul_f32 v[130:131], v[110:111], v[128:129] op_sel:[1,0]
	v_pk_mul_f32 v[134:135], v[116:117], v[128:129] op_sel_hi:[0,1]
	v_pk_mul_f32 v[142:143], v[116:117], v[128:129] op_sel:[1,0]
	v_pk_fma_f32 v[130:131], v[116:117], v[68:69], v[130:131] op_sel_hi:[0,1,1]
	v_pk_fma_f32 v[134:135], v[118:119], v[68:69], v[134:135] op_sel_hi:[0,1,1]
	v_pk_fma_f32 v[142:143], v[118:119], v[68:69], v[142:143] op_sel:[1,0,0]
	v_pk_fma_f32 v[130:131], v[116:117], v[100:101], v[130:131] op_sel:[1,0,0]
	v_pk_fma_f32 v[134:135], v[118:119], v[100:101], v[134:135] op_sel:[1,0,0]
	v_pk_fma_f32 v[142:143], v[120:121], v[100:101], v[142:143] op_sel_hi:[0,1,1]
	v_pk_mul_f32 v[132:133], v[108:109], v[130:131] op_sel_hi:[0,1]
	v_pk_fma_f32 v[132:133], v[108:109], v[134:135], v[132:133] op_sel:[1,0,0]
	v_pk_fma_f32 v[132:133], v[110:111], v[142:143], v[132:133] op_sel_hi:[0,1,1]
	v_pk_fma_f32 v[132:133], v[120:121], v[90:91], v[132:133] op_sel:[1,0,0] neg_lo:[0,0,1] neg_hi:[0,0,1]
	v_cmp_eq_u32_e64 s[10:11], 6, v123
	v_cmp_eq_u32_e64 s[14:15], 7, v123
	v_pk_add_f32 v[68:69], v[60:61], v[130:131]
	v_pk_add_f32 v[90:91], v[98:99], v[68:69]
	v_pk_add_f32 v[60:61], v[88:89], v[134:135]
	v_pk_add_f32 v[98:99], v[102:103], v[60:61]
	v_pk_add_f32 v[88:89], v[92:93], v[142:143]
	v_pk_add_f32 v[100:101], v[106:107], v[88:89]
	v_pk_add_f32 v[102:103], v[50:51], v[132:133]
	v_pk_add_f32 v[92:93], v[72:73], v[102:103]
	v_pk_fma_f32 v[72:73], v[12:13], v[90:91], v[92:93] op_sel_hi:[0,1,1]
	v_pk_fma_f32 v[128:129], v[64:65], v[90:91], v[92:93] op_sel_hi:[0,1,1]
	v_pk_fma_f32 v[72:73], v[12:13], v[98:99], v[72:73] op_sel:[1,0,0]
	v_pk_fma_f32 v[128:129], v[64:65], v[98:99], v[128:129] op_sel:[1,0,0]
	v_pk_fma_f32 v[72:73], v[14:15], v[100:101], v[72:73] op_sel_hi:[0,1,1]
	v_pk_fma_f32 v[128:129], v[66:67], v[100:101], v[128:129] op_sel_hi:[0,1,1]
	v_pk_fma_f32 v[92:93], v[156:157], v[90:91], v[92:93] op_sel_hi:[0,1,1]
	v_pk_fma_f32 v[92:93], v[156:157], v[98:99], v[92:93] op_sel:[1,0,0]
	v_pk_fma_f32 v[92:93], v[158:159], v[100:101], v[92:93] op_sel_hi:[0,1,1]
	v_cndmask_b32_e64 v50, 0, v18, s[10:11]
	v_cndmask_b32_e64 v51, 0, v18, s[14:15]
	v_add_f32_dpp v92, v72, v92 wave_shl:1 row_mask:0xf bank_mask:0xf bound_ctrl:1
	v_add_f32_dpp v93, v73, v93 wave_shl:1 row_mask:0xf bank_mask:0xf bound_ctrl:1
	s_add_i32 s4, s34, 8
	s_cmpk_lt_i32 s4, 0x201
	s_cselect_b64 s[12:13], s[0:1], 0
	v_add_f32_dpp v92, v128, v92 wave_shr:1 row_mask:0xf bank_mask:0xf bound_ctrl:1
	v_add_f32_dpp v93, v129, v93 wave_shr:1 row_mask:0xf bank_mask:0xf bound_ctrl:1
	v_pk_fma_f32 v[92:93], v[52:53], v[122:123], v[92:93] op_sel_hi:[1,0,1] neg_lo:[0,0,1] neg_hi:[0,0,1]
	v_pk_add_f32 v[92:93], v[92:93], v[50:51] neg_lo:[0,1] neg_hi:[0,1]
	v_pk_mul_f32 v[106:107], v[92:93], v[92:93]
	v_add_f32_e32 v106, v106, v107
	v_cndmask_b32_e64 v107, 0, v106, s[12:13]
	v_add_f32_e32 v1, v1, v107
	s_waitcnt vmcnt(0)
	v_mov_b32_dpp v12, v160 wave_shr:1 row_mask:0xf bank_mask:0xf bound_ctrl:1
	v_mov_b32_dpp v13, v161 wave_shr:1 row_mask:0xf bank_mask:0xf bound_ctrl:1
	v_mov_b32_dpp v14, v162 wave_shr:1 row_mask:0xf bank_mask:0xf bound_ctrl:1
	v_mov_b32_dpp v64, v160 wave_shl:1 row_mask:0xf bank_mask:0xf bound_ctrl:1
	v_mov_b32_dpp v65, v161 wave_shl:1 row_mask:0xf bank_mask:0xf bound_ctrl:1
	v_mov_b32_dpp v66, v162 wave_shl:1 row_mask:0xf bank_mask:0xf bound_ctrl:1
	v_pk_add_f32 v[50:51], v[160:161], v[12:13]
	v_pk_mul_f32 v[52:53], v[160:161], v[160:161] op_sel_hi:[0,1]
	v_pk_mul_f32 v[72:73], v[160:161], v[162:163] op_sel_hi:[1,0]
	v_mul_f32_e64 v90, v161, v161
	v_mul_f32_e64 v91, v162, v162
	v_add_f32_e64 v92, v162, v14
	v_pk_add_f32 v[50:51], v[50:51], v[64:65]
	v_or3_b32 v17, v29, v56, v59
	v_or3_b32 v17, v17, v78, v79
	s_add_i32 s4, s34, 9
	s_cmpk_lt_u32 s4, 0x1ff
	s_cselect_b64 s[12:13], s[42:43], 0
	v_cmp_ne_u32_e64 s[30:31], 0, v17
	s_and_b64 s[30:31], s[30:31], s[12:13]
	v_cndmask_b32_e64 v17, 0, 1.0, s[30:31]
	v_pk_fma_f32 v[52:53], v[12:13], v[12:13], v[52:53] op_sel_hi:[0,1,1]
	v_pk_fma_f32 v[72:73], v[12:13], v[14:15], v[72:73] op_sel_hi:[1,0,1]
	v_fma_f32 v90, v13, v13, v90
	v_fma_f32 v91, v14, v14, v91
	v_add_f32_dpp v93, v17, v17 wave_shr:1 row_mask:0xf bank_mask:0xf bound_ctrl:1
	v_add_f32_e64 v92, v92, v66
	v_pk_fma_f32 v[52:53], v[64:65], v[64:65], v[52:53] op_sel_hi:[0,1,1]
	v_pk_fma_f32 v[72:73], v[64:65], v[66:67], v[72:73] op_sel_hi:[1,0,1]
	v_fma_f32 v90, v65, v65, v90
	v_fma_f32 v91, v66, v66, v91
	v_add_f32_dpp v93, v17, v93 wave_shl:1 row_mask:0xf bank_mask:0xf bound_ctrl:1
	v_pk_add_f32 v[98:99], v[80:81], v[50:51]
	v_pk_add_f32 v[80:81], v[6:7], v[52:53]
	v_pk_add_f32 v[6:7], v[20:21], v[72:73]
	v_pk_add_f32 v[20:21], v[46:47], v[90:91]
	v_pk_add_f32 v[46:47], v[76:77], v[92:93]
	v_mul_f32_e64 v108, v98, v22
	v_mul_f32_e64 v109, v99, v22
	v_mul_f32_e64 v110, v46, v22
	v_fma_f32 v17, v80, v22, v26
	v_mul_f32_e64 v25, v81, v22
	v_mul_f32_e64 v57, v6, v22
	v_fma_f32 v58, v20, v22, v26
	v_mul_f32_e64 v76, v7, v22
	v_fma_f32 v77, v21, v22, v26
	v_fma_f32 v17, -v108, v108, v17
	v_fma_f32 v25, -v108, v109, v25
	v_fma_f32 v57, -v108, v110, v57
	v_fma_f32 v58, -v109, v109, v58
	v_fma_f32 v76, -v109, v110, v76
	v_fma_f32 v77, -v110, v110, v77
	v_mul_f32_e64 v100, v76, v76
	v_mul_f32_e64 v101, v25, v77
	v_mul_f32_e64 v106, v57, v58
	v_mul_f32_e64 v107, v57, v57
	v_mul_f32_e64 v128, v17, v76
	v_mul_f32_e64 v129, v25, v25
	v_fma_f32 v100, v58, v77, -v100
	v_fma_f32 v101, v57, v76, -v101
	v_fma_f32 v106, v25, v76, -v106
	v_fma_f32 v107, v17, v77, -v107
	v_fma_f32 v128, v25, v57, -v128
	v_fma_f32 v129, v17, v58, -v129
	v_mul_f32_e64 v140, v17, v100
	v_fma_f32 v140, v25, v101, v140
	v_fma_f32 v140, v57, v106, v140
	v_rcp_f32_e32 v140, v140
	v_cmp_ne_u32_e64 vcc, s37, v24
	v_mul_f32_e64 v140, v140, v22
	v_cndmask_b32_e64 v140, 0, v140, s[30:31]
	v_cndmask_b32_e64 v17, 0, v18, vcc
	v_cndmask_b32_e64 v121, 0, v22, s[30:31]
	v_mul_f32_e64 v111, v100, v140
	v_mul_f32_e64 v116, v101, v140
	v_mul_f32_e64 v117, v106, v140
	v_mul_f32_e64 v118, v107, v140
	v_mul_f32_e64 v119, v128, v140
	v_mul_f32_e64 v120, v129, v140
	v_add_f32_e64 v122, v47, v17
	v_mov_b32_e32 v123, v24
	ds_write_b128 v23, v[108:111] offset:3072
	ds_write_b128 v23, v[116:119] offset:4096
	ds_write_b128 v23, v[120:123] offset:5120
	v_mov_b32_dpp v20, v54 wave_shr:1 row_mask:0xf bank_mask:0xf bound_ctrl:1
	v_mov_b32_dpp v21, v55 wave_shr:1 row_mask:0xf bank_mask:0xf bound_ctrl:1
	v_mov_b32_dpp v24, v54 wave_shl:1 row_mask:0xf bank_mask:0xf bound_ctrl:1
	v_mov_b32_dpp v25, v55 wave_shl:1 row_mask:0xf bank_mask:0xf bound_ctrl:1
	v_pk_mul_f32 v[6:7], v[54:55], v[160:161] op_sel_hi:[1,0]
	v_pk_mul_f32 v[46:47], v[54:55], v[160:161] op_sel:[0,1]
	v_pk_mul_f32 v[98:99], v[54:55], v[162:163] op_sel_hi:[1,0]
	v_pk_add_f32 v[106:107], v[54:55], v[20:21]
	v_pk_fma_f32 v[6:7], v[20:21], v[12:13], v[6:7] op_sel_hi:[1,0,1]
	v_pk_fma_f32 v[46:47], v[20:21], v[12:13], v[46:47] op_sel:[0,1,0]
	v_pk_fma_f32 v[98:99], v[20:21], v[14:15], v[98:99] op_sel_hi:[1,0,1]
	v_pk_add_f32 v[106:107], v[106:107], v[24:25]
	v_pk_fma_f32 v[6:7], v[24:25], v[64:65], v[6:7] op_sel_hi:[1,0,1]
	v_pk_fma_f32 v[46:47], v[24:25], v[64:65], v[46:47] op_sel:[0,1,0]
	v_pk_fma_f32 v[98:99], v[24:25], v[66:67], v[98:99] op_sel_hi:[1,0,1]
	s_waitcnt lgkmcnt(0)
	s_barrier
	v_pk_add_f32 v[20:21], v[82:83], v[106:107]
	v_pk_add_f32 v[82:83], v[94:95], v[6:7]
	v_pk_add_f32 v[94:95], v[74:75], v[46:47]
	v_pk_add_f32 v[74:75], v[114:115], v[98:99]
	v_pk_fma_f32 v[82:83], v[108:109], v[20:21], v[82:83] op_sel_hi:[0,1,1] neg_lo:[1,0,0] neg_hi:[1,0,0]
	v_pk_fma_f32 v[94:95], v[108:109], v[20:21], v[94:95] op_sel:[1,0,0] neg_lo:[1,0,0] neg_hi:[1,0,0]
	v_pk_fma_f32 v[74:75], v[110:111], v[20:21], v[74:75] op_sel_hi:[0,1,1] neg_lo:[1,0,0] neg_hi:[1,0,0]
	v_pk_mul_f32 v[24:25], v[110:111], v[82:83] op_sel:[1,0]
	v_pk_mul_f32 v[76:77], v[116:117], v[82:83] op_sel_hi:[0,1]
	v_pk_mul_f32 v[80:81], v[116:117], v[82:83] op_sel:[1,0]
	v_pk_fma_f32 v[24:25], v[116:117], v[94:95], v[24:25] op_sel_hi:[0,1,1]
	v_pk_fma_f32 v[76:77], v[118:119], v[94:95], v[76:77] op_sel_hi:[0,1,1]
	v_pk_fma_f32 v[80:81], v[118:119], v[94:95], v[80:81] op_sel:[1,0,0]
	v_pk_fma_f32 v[24:25], v[116:117], v[74:75], v[24:25] op_sel:[1,0,0]
	v_pk_fma_f32 v[76:77], v[118:119], v[74:75], v[76:77] op_sel:[1,0,0]
	v_pk_fma_f32 v[80:81], v[120:121], v[74:75], v[80:81] op_sel_hi:[0,1,1]
	v_pk_mul_f32 v[114:115], v[108:109], v[24:25] op_sel_hi:[0,1]
	v_pk_fma_f32 v[114:115], v[108:109], v[76:77], v[114:115] op_sel:[1,0,0]
	v_pk_fma_f32 v[114:115], v[110:111], v[80:81], v[114:115] op_sel_hi:[0,1,1]
	v_pk_fma_f32 v[114:115], v[120:121], v[20:21], v[114:115] op_sel:[1,0,0] neg_lo:[0,0,1] neg_hi:[0,0,1]
	v_cmp_eq_u32_e64 s[10:11], 6, v123
	v_cmp_eq_u32_e64 s[14:15], 7, v123
	v_pk_add_f32 v[20:21], v[68:69], v[24:25]
	v_pk_add_f32 v[68:69], v[60:61], v[76:77]
	v_pk_add_f32 v[60:61], v[88:89], v[80:81]
	v_pk_add_f32 v[74:75], v[102:103], v[114:115]
	v_pk_fma_f32 v[82:83], v[32:33], v[20:21], v[74:75] op_sel_hi:[0,1,1]
	v_pk_fma_f32 v[94:95], v[84:85], v[20:21], v[74:75] op_sel_hi:[0,1,1]
	v_pk_fma_f32 v[82:83], v[32:33], v[68:69], v[82:83] op_sel:[1,0,0]
	v_pk_fma_f32 v[94:95], v[84:85], v[68:69], v[94:95] op_sel:[1,0,0]
	v_pk_fma_f32 v[82:83], v[34:35], v[60:61], v[82:83] op_sel_hi:[0,1,1]
	v_pk_fma_f32 v[94:95], v[86:87], v[60:61], v[94:95] op_sel_hi:[0,1,1]
	v_pk_fma_f32 v[74:75], v[124:125], v[20:21], v[74:75] op_sel_hi:[0,1,1]
	v_pk_fma_f32 v[74:75], v[124:125], v[68:69], v[74:75] op_sel:[1,0,0]
	v_pk_fma_f32 v[74:75], v[126:127], v[60:61], v[74:75] op_sel_hi:[0,1,1]
	v_cndmask_b32_e64 v88, 0, v18, s[10:11]
	v_cndmask_b32_e64 v89, 0, v18, s[14:15]
	v_add_f32_dpp v74, v82, v74 wave_shl:1 row_mask:0xf bank_mask:0xf bound_ctrl:1
	v_add_f32_dpp v75, v83, v75 wave_shl:1 row_mask:0xf bank_mask:0xf bound_ctrl:1
	s_add_i32 s4, s34, 9
	s_cmpk_lt_i32 s4, 0x201
	s_cselect_b64 s[12:13], s[0:1], 0
	v_add_f32_dpp v74, v94, v74 wave_shr:1 row_mask:0xf bank_mask:0xf bound_ctrl:1
	v_add_f32_dpp v75, v95, v75 wave_shr:1 row_mask:0xf bank_mask:0xf bound_ctrl:1
	v_pk_fma_f32 v[74:75], v[30:31], v[122:123], v[74:75] op_sel_hi:[1,0,1] neg_lo:[0,0,1] neg_hi:[0,0,1]
	v_pk_add_f32 v[74:75], v[74:75], v[88:89] neg_lo:[0,1] neg_hi:[0,1]
	v_pk_mul_f32 v[100:101], v[74:75], v[74:75]
	v_add_f32_e32 v100, v100, v101
	v_cndmask_b32_e64 v101, 0, v100, s[12:13]
	v_add_f32_e32 v1, v1, v101
	v_mov_b32_e32 v0, v1
	s_branch .LBB0_29
